# s29
# baseline (speedup 1.0000x reference)
.LBB1_5:
	v_lshlrev_b32_e32 v67, 4, v1
	v_lshrrev_b32_e32 v1, 1, v1
	v_lshrrev_b32_e32 v69, 5, v132
	v_ashrrev_i32_e32 v66, 4, v132
	v_bitop3_b32 v1, v1, v69, 7 bitop3:0x78
	s_add_u32 s22, s24, s2
	v_lshlrev_b32_e32 v68, 7, v66
	v_lshlrev_b32_e32 v1, 4, v1
	v_and_b32_e32 v0, 8, v0
	s_addc_u32 s90, s25, s3
	v_lshl_or_b32 v201, v66, 12, v67
	v_or3_b32 v0, v68, v1, v0
	v_add_u32_e32 v100, 0x10000, v0
	v_cvt_pk_f16_f32 v1, v64, v65
	v_cvt_pk_f16_f32 v0, v62, v63
	v_cvt_pk_f16_f32 v61, v60, v61
	v_cvt_pk_f16_f32 v60, v58, v59
	ds_write2st64_b64 v100, v[0:1], v[60:61] offset1:8
	v_cvt_pk_f16_f32 v1, v56, v57
	v_cvt_pk_f16_f32 v0, v54, v55
	v_cvt_pk_f16_f32 v53, v52, v53
	v_cvt_pk_f16_f32 v52, v50, v51
	ds_write2st64_b64 v100, v[0:1], v[52:53] offset0:16 offset1:24
	v_cvt_pk_f16_f32 v1, v48, v49
	v_cvt_pk_f16_f32 v0, v46, v47
	v_cvt_pk_f16_f32 v45, v44, v45
	v_cvt_pk_f16_f32 v44, v42, v43
	ds_write2st64_b64 v100, v[0:1], v[44:45] offset0:32 offset1:40
	v_cvt_pk_f16_f32 v1, v40, v41
	v_cvt_pk_f16_f32 v0, v38, v39
	v_cvt_pk_f16_f32 v37, v36, v37
	v_cvt_pk_f16_f32 v36, v34, v35
	ds_write2st64_b64 v100, v[0:1], v[36:37] offset0:48 offset1:56
	s_add_u32 s0, s22, 0x200
	s_addc_u32 s1, s90, 0
	s_add_u32 s70, s0, 0x20000
	s_addc_u32 s71, s1, 0
	s_add_u32 s72, s0, 0x40000
	s_addc_u32 s73, s1, 0
	s_add_u32 s92, s0, 0x60000
	s_addc_u32 s93, s1, 0
	s_add_u32 s94, s0, 0x80000
	s_addc_u32 s95, s1, 0
	s_add_u32 s96, s0, 0xa0000
	s_addc_u32 s97, s1, 0
	s_add_u32 s98, s0, 0xc0000
	s_addc_u32 s99, s1, 0
	s_add_u32 s80, s0, 0xe0000
	s_addc_u32 s81, s1, 0
	global_load_dwordx4 v[70:73], v201, s[0:1] nt
	global_load_dwordx4 v[42:45], v201, s[70:71] nt
	global_load_dwordx4 v[46:49], v201, s[72:73] nt
	global_load_dwordx4 v[66:69], v201, s[92:93] nt
	global_load_dwordx4 v[62:65], v201, s[94:95] nt
	global_load_dwordx4 v[58:61], v201, s[96:97] nt
	global_load_dwordx4 v[54:57], v201, s[98:99] nt
	global_load_dwordx4 v[50:53], v201, s[80:81] nt
	s_waitcnt vmcnt(8)
	s_waitcnt lgkmcnt(0)
	s_barrier
	ds_read_b128 v[34:37], v131
	ds_read_b128 v[38:41], v131 offset:2048
	ds_read_b128 v[74:77], v131 offset:4096
	ds_read_b128 v[78:81], v131 offset:6144
	ds_read_b128 v[82:85], v129
	ds_read_b128 v[86:89], v129 offset:2048
	s_add_u32 s70, s22, 0x300
	v_add_u32_e32 v95, 0x8000, v94
	v_lshl_add_u64 v[0:1], s[26:27], 0, v[196:197]
	s_addc_u32 s71, s90, 0
	v_readfirstlane_b32 s0, v95
	s_mov_b32 m0, s0
	v_cvt_pk_f16_f32 v33, v32, v33
	global_load_lds_dwordx4 v[0:1], off
	v_cvt_pk_f16_f32 v32, v30, v31
	ds_write_b64 v100, v[32:33] offset:32768
	s_setprio 1
	s_waitcnt lgkmcnt(1)
	v_mfma_f32_16x16x32_f16 v[90:93], v[82:85], v[34:37], 0
	v_mfma_f32_16x16x32_f16 v[102:105], v[82:85], v[38:41], 0
	v_mfma_f32_16x16x32_f16 v[106:109], v[82:85], v[74:77], 0
	v_mfma_f32_16x16x32_f16 v[82:85], v[82:85], v[78:81], 0
	v_mfma_f32_16x16x32_f16 v[110:113], v[86:89], v[34:37], 0
	v_mfma_f32_16x16x32_f16 v[114:117], v[86:89], v[38:41], 0
	v_mfma_f32_16x16x32_f16 v[118:121], v[86:89], v[74:77], 0
	v_mfma_f32_16x16x32_f16 v[86:89], v[86:89], v[78:81], 0
	s_setprio 0
	ds_read_b128 v[122:125], v129 offset:4096
	ds_read_b128 v[134:137], v129 offset:6144
	v_add_u32_e32 v96, 0xa000, v94
	v_lshl_add_u64 v[98:99], v[0:1], 0, s[58:59]
	v_readfirstlane_b32 s1, v96
	s_mov_b32 m0, s1
	v_cvt_pk_f16_f32 v29, v28, v29
	global_load_lds_dwordx4 v[98:99], off
	v_cvt_pk_f16_f32 v28, v26, v27
	ds_write_b64 v100, v[28:29] offset:36864
	s_add_u32 s70, s22, 0x20300
	s_addc_u32 s71, s90, 0
	s_setprio 1
	s_waitcnt lgkmcnt(1)
	v_mfma_f32_16x16x32_f16 v[138:141], v[122:125], v[34:37], 0
	v_mfma_f32_16x16x32_f16 v[142:145], v[122:125], v[38:41], 0
	v_mfma_f32_16x16x32_f16 v[146:149], v[122:125], v[74:77], 0
	v_mfma_f32_16x16x32_f16 v[122:125], v[122:125], v[78:81], 0
	v_mfma_f32_16x16x32_f16 v[150:153], v[134:137], v[34:37], 0
	v_mfma_f32_16x16x32_f16 v[154:157], v[134:137], v[38:41], 0
	v_mfma_f32_16x16x32_f16 v[158:161], v[134:137], v[74:77], 0
	v_mfma_f32_16x16x32_f16 v[134:137], v[134:137], v[78:81], 0
	s_setprio 0
	ds_read_b128 v[162:165], v129 offset:8192
	ds_read_b128 v[166:169], v129 offset:10240
	v_add_u32_e32 v97, 0xc000, v94
	v_lshl_add_u64 v[98:99], v[0:1], 0, s[60:61]
	v_readfirstlane_b32 s71, v97
	s_mov_b32 m0, s71
	v_cvt_pk_f16_f32 v25, v24, v25
	global_load_lds_dwordx4 v[98:99], off
	v_cvt_pk_f16_f32 v24, v22, v23
	ds_write_b64 v100, v[24:25] offset:40960
	s_add_u32 s72, s22, 0x40300
	s_addc_u32 s73, s90, 0
	s_add_u32 s100, s22, 0x300
	s_addc_u32 s101, s90, 0
	global_load_dwordx4 v[30:33], v201, s[100:101] nt
	s_setprio 1
	s_waitcnt lgkmcnt(1)
	v_mfma_f32_16x16x32_f16 v[170:173], v[162:165], v[34:37], 0
	v_mfma_f32_16x16x32_f16 v[174:177], v[162:165], v[38:41], 0
	v_mfma_f32_16x16x32_f16 v[178:181], v[162:165], v[74:77], 0
	v_mfma_f32_16x16x32_f16 v[162:165], v[162:165], v[78:81], 0
	v_mfma_f32_16x16x32_f16 v[182:185], v[166:169], v[34:37], 0
	v_mfma_f32_16x16x32_f16 v[186:189], v[166:169], v[38:41], 0
	v_mfma_f32_16x16x32_f16 v[190:193], v[166:169], v[74:77], 0
	v_mfma_f32_16x16x32_f16 v[166:169], v[166:169], v[78:81], 0
	s_setprio 0
	ds_read_b128 v[202:205], v129 offset:12288
	ds_read_b128 v[206:209], v129 offset:14336
	v_add_u32_e32 v98, 0xe000, v94
	v_lshl_add_u64 v[0:1], v[0:1], 0, s[62:63]
	v_readfirstlane_b32 s72, v98
	s_mov_b32 m0, s72
	s_nop 0
	global_load_lds_dwordx4 v[0:1], off
	v_cvt_pk_f16_f32 v1, v20, v21
	v_cvt_pk_f16_f32 v0, v18, v19
	ds_write_b64 v100, v[0:1] offset:45056
	s_add_u32 s80, s22, 0x60300
	s_addc_u32 s81, s90, 0
	s_add_u32 s100, s22, 0x20300
	s_addc_u32 s101, s90, 0
	global_load_dwordx4 v[26:29], v201, s[100:101] nt
	s_setprio 1
	s_waitcnt lgkmcnt(1)
	v_mfma_f32_16x16x32_f16 v[210:213], v[202:205], v[34:37], 0
	v_mfma_f32_16x16x32_f16 v[214:217], v[202:205], v[38:41], 0
	v_mfma_f32_16x16x32_f16 v[218:221], v[202:205], v[74:77], 0
	v_mfma_f32_16x16x32_f16 v[202:205], v[202:205], v[78:81], 0
	v_mfma_f32_16x16x32_f16 v[74:77], v[206:209], v[74:77], 0
	v_mfma_f32_16x16x32_f16 v[78:81], v[206:209], v[78:81], 0
	v_mfma_f32_16x16x32_f16 v[222:225], v[206:209], v[34:37], 0
	v_mfma_f32_16x16x32_f16 v[226:229], v[206:209], v[38:41], 0
	s_setprio 0
	ds_read_b128 v[206:209], v128
	ds_read_b128 v[230:233], v128 offset:2048
	ds_read_b128 v[234:237], v128 offset:4096
	ds_read_b128 v[238:241], v128 offset:6144
	ds_read_b128 v[34:37], v130
	ds_read_b128 v[38:41], v130 offset:2048
	v_cvt_pk_f16_f32 v1, v16, v17
	v_cvt_pk_f16_f32 v0, v14, v15
	ds_write_b64 v100, v[0:1] offset:49152
	s_add_u32 s80, s22, 0x80300
	s_addc_u32 s81, s90, 0
	s_add_u32 s100, s22, 0x40300
	s_addc_u32 s101, s90, 0
	global_load_dwordx4 v[22:25], v201, s[100:101] nt
	s_setprio 1
	s_waitcnt lgkmcnt(1)
	v_mfma_f32_16x16x32_f16 v[90:93], v[34:37], v[206:209], v[90:93]
	v_mfma_f32_16x16x32_f16 v[102:105], v[34:37], v[230:233], v[102:105]
	v_mfma_f32_16x16x32_f16 v[106:109], v[34:37], v[234:237], v[106:109]
	v_mfma_f32_16x16x32_f16 v[82:85], v[34:37], v[238:241], v[82:85]
	v_mfma_f32_16x16x32_f16 v[110:113], v[38:41], v[206:209], v[110:113]
	v_mfma_f32_16x16x32_f16 v[114:117], v[38:41], v[230:233], v[114:117]
	v_mfma_f32_16x16x32_f16 v[118:121], v[38:41], v[234:237], v[118:121]
	v_mfma_f32_16x16x32_f16 v[86:89], v[38:41], v[238:241], v[86:89]
	s_setprio 0
	ds_read_b128 v[34:37], v130 offset:4096
	ds_read_b128 v[38:41], v130 offset:6144
	v_cvt_pk_f16_f32 v1, v12, v13
	v_cvt_pk_f16_f32 v0, v10, v11
	ds_write_b64 v100, v[0:1] offset:53248
	s_add_u32 s80, s22, 0xa0300
	s_addc_u32 s81, s90, 0
	s_add_u32 s100, s22, 0x60300
	s_addc_u32 s101, s90, 0
	global_load_dwordx4 v[18:21], v201, s[100:101] nt
	s_setprio 1
	s_waitcnt lgkmcnt(1)
	v_mfma_f32_16x16x32_f16 v[146:149], v[34:37], v[234:237], v[146:149]
	v_mfma_f32_16x16x32_f16 v[122:125], v[34:37], v[238:241], v[122:125]
	v_mfma_f32_16x16x32_f16 v[134:137], v[38:41], v[238:241], v[134:137]
	v_mfma_f32_16x16x32_f16 v[138:141], v[34:37], v[206:209], v[138:141]
	v_mfma_f32_16x16x32_f16 v[142:145], v[34:37], v[230:233], v[142:145]
	v_mfma_f32_16x16x32_f16 v[150:153], v[38:41], v[206:209], v[150:153]
	v_mfma_f32_16x16x32_f16 v[154:157], v[38:41], v[230:233], v[154:157]
	v_mfma_f32_16x16x32_f16 v[158:161], v[38:41], v[234:237], v[158:161]
	s_setprio 0
	ds_read_b128 v[38:41], v130 offset:8192
	ds_read_b128 v[242:245], v130 offset:10240
	v_cvt_pk_f16_f32 v1, v8, v9
	v_cvt_pk_f16_f32 v0, v6, v7
	ds_write_b64 v100, v[0:1] offset:57344
	s_add_u32 s80, s22, 0xc0300
	s_addc_u32 s81, s90, 0
	s_add_u32 s100, s22, 0x80300
	s_addc_u32 s101, s90, 0
	global_load_dwordx4 v[14:17], v201, s[100:101] nt
	s_add_u32 s100, s22, 0xa0300
	s_addc_u32 s101, s90, 0
	global_load_dwordx4 v[10:13], v201, s[100:101] nt
	s_setprio 1
	s_waitcnt lgkmcnt(1)
	v_mfma_f32_16x16x32_f16 v[6:9], v[38:41], v[206:209], v[170:173]
	v_mfma_f32_16x16x32_f16 v[170:173], v[38:41], v[230:233], v[174:177]
	v_mfma_f32_16x16x32_f16 v[174:177], v[38:41], v[234:237], v[178:181]
	v_mfma_f32_16x16x32_f16 v[162:165], v[38:41], v[238:241], v[162:165]
	v_mfma_f32_16x16x32_f16 v[178:181], v[242:245], v[206:209], v[182:185]
	v_mfma_f32_16x16x32_f16 v[182:185], v[242:245], v[230:233], v[186:189]
	v_mfma_f32_16x16x32_f16 v[186:189], v[242:245], v[234:237], v[190:193]
	v_mfma_f32_16x16x32_f16 v[166:169], v[242:245], v[238:241], v[166:169]
	s_setprio 0
	s_nop 0
	ds_read_b128 v[190:193], v130 offset:12288
	ds_read_b128 v[242:245], v130 offset:14336
	v_cvt_pk_f16_f32 v1, v4, v5
	v_cvt_pk_f16_f32 v0, v2, v3
	ds_write_b64 v100, v[0:1] offset:61440
	s_add_u32 s80, s22, 0xe0300
	s_addc_u32 s81, s90, 0
	s_add_u32 s100, s22, 0xc0300
	s_addc_u32 s101, s90, 0
	global_load_dwordx4 v[34:37], v201, s[100:101] nt
	s_add_u32 s100, s22, 0xe0300
	s_addc_u32 s101, s90, 0
	global_load_dwordx4 v[38:41], v201, s[100:101] nt
	s_setprio 1
	s_waitcnt lgkmcnt(1)
	v_mfma_f32_16x16x32_f16 v[78:81], v[242:245], v[238:241], v[78:81]
	v_mfma_f32_16x16x32_f16 v[210:213], v[190:193], v[206:209], v[210:213]
	v_mfma_f32_16x16x32_f16 v[214:217], v[190:193], v[230:233], v[214:217]
	v_mfma_f32_16x16x32_f16 v[218:221], v[190:193], v[234:237], v[218:221]
	v_mfma_f32_16x16x32_f16 v[190:193], v[190:193], v[238:241], v[202:205]
	v_mfma_f32_16x16x32_f16 v[202:205], v[242:245], v[206:209], v[222:225]
	v_mfma_f32_16x16x32_f16 v[206:209], v[242:245], v[230:233], v[226:229]
	v_mfma_f32_16x16x32_f16 v[222:225], v[242:245], v[234:237], v[74:77]
	s_setprio 0
	s_waitcnt vmcnt(7)
	s_waitcnt lgkmcnt(0)
	s_barrier
	ds_read_b128 v[226:229], v131 offset:32768
	ds_read_b128 v[230:233], v131 offset:34816
	ds_read_b128 v[234:237], v131 offset:36864
	ds_read_b128 v[238:241], v131 offset:38912
	ds_read_b128 v[74:77], v129 offset:32768
	ds_read_b128 v[242:245], v129 offset:34816
	s_add_u32 s80, s22, 0x400
	s_addc_u32 s81, s90, 0
	v_lshl_add_u64 v[198:199], s[28:29], 0, v[196:197]
	v_readfirstlane_b32 s70, v94
	s_mov_b32 m0, s70
	v_cvt_pk_f16_f32 v1, v72, v73
	global_load_lds_dwordx4 v[198:199], off
	v_cvt_pk_f16_f32 v0, v70, v71
	ds_write_b64 v100, v[0:1]
	s_setprio 1
	s_waitcnt lgkmcnt(1)
	v_mfma_f32_16x16x32_f16 v[70:73], v[74:77], v[226:229], v[90:93]
	v_mfma_f32_16x16x32_f16 v[90:93], v[74:77], v[230:233], v[102:105]
	v_mfma_f32_16x16x32_f16 v[104:107], v[74:77], v[234:237], v[106:109]
	v_mfma_f32_16x16x32_f16 v[82:85], v[74:77], v[238:241], v[82:85]
	v_mfma_f32_16x16x32_f16 v[108:111], v[242:245], v[226:229], v[110:113]
	v_mfma_f32_16x16x32_f16 v[112:115], v[242:245], v[230:233], v[114:117]
	v_mfma_f32_16x16x32_f16 v[116:119], v[242:245], v[234:237], v[118:121]
	v_mfma_f32_16x16x32_f16 v[86:89], v[242:245], v[238:241], v[86:89]
	s_setprio 0
	ds_read_b128 v[74:77], v129 offset:36864
	ds_read_b128 v[242:245], v129 offset:38912
	v_add_u32_e32 v99, 0x2000, v94
	v_lshl_add_u64 v[4:5], v[198:199], 0, s[58:59]
	v_readfirstlane_b32 s73, v99
	s_mov_b32 m0, s73
	s_nop 0
	global_load_lds_dwordx4 v[4:5], off
	v_cvt_pk_f16_f32 v5, v44, v45
	v_cvt_pk_f16_f32 v4, v42, v43
	ds_write_b64 v100, v[4:5] offset:4096
	s_add_u32 s80, s22, 0x20400
	s_addc_u32 s81, s90, 0
	s_setprio 1
	s_waitcnt lgkmcnt(1)
	v_mfma_f32_16x16x32_f16 v[146:149], v[74:77], v[234:237], v[146:149]
	v_mfma_f32_16x16x32_f16 v[120:123], v[74:77], v[238:241], v[122:125]
	v_mfma_f32_16x16x32_f16 v[124:127], v[242:245], v[226:229], v[150:153]
	v_mfma_f32_16x16x32_f16 v[134:137], v[242:245], v[238:241], v[134:137]
	v_mfma_f32_16x16x32_f16 v[138:141], v[74:77], v[226:229], v[138:141]
	v_mfma_f32_16x16x32_f16 v[142:145], v[74:77], v[230:233], v[142:145]
	v_mfma_f32_16x16x32_f16 v[150:153], v[242:245], v[230:233], v[154:157]
	v_mfma_f32_16x16x32_f16 v[154:157], v[242:245], v[234:237], v[158:161]
	s_setprio 0
	ds_read_b128 v[74:77], v129 offset:40960
	s_nop 0
	ds_read_b128 v[158:161], v129 offset:43008
	v_add_u32_e32 v101, 0x4000, v94
	v_lshl_add_u64 v[4:5], v[198:199], 0, s[60:61]
	v_readfirstlane_b32 s91, v101
	s_mov_b32 m0, s91
	s_nop 0
	global_load_lds_dwordx4 v[4:5], off
	v_cvt_pk_f16_f32 v5, v48, v49
	v_cvt_pk_f16_f32 v4, v46, v47
	ds_write_b64 v100, v[4:5] offset:8192
	s_add_u32 s80, s22, 0x40400
	s_addc_u32 s81, s90, 0
	s_add_u32 s100, s22, 0x400
	s_addc_u32 s101, s90, 0
	global_load_dwordx4 v[0:3], v201, s[100:101] nt
	s_setprio 1
	s_waitcnt lgkmcnt(1)
	v_mfma_f32_16x16x32_f16 v[4:7], v[74:77], v[226:229], v[6:9]
	v_mfma_f32_16x16x32_f16 v[170:173], v[74:77], v[230:233], v[170:173]
	v_mfma_f32_16x16x32_f16 v[174:177], v[74:77], v[234:237], v[174:177]
	v_mfma_f32_16x16x32_f16 v[162:165], v[74:77], v[238:241], v[162:165]
	v_mfma_f32_16x16x32_f16 v[178:181], v[158:161], v[226:229], v[178:181]
	v_mfma_f32_16x16x32_f16 v[182:185], v[158:161], v[230:233], v[182:185]
	v_mfma_f32_16x16x32_f16 v[186:189], v[158:161], v[234:237], v[186:189]
	v_mfma_f32_16x16x32_f16 v[158:161], v[158:161], v[238:241], v[166:169]
	s_setprio 0
	s_nop 1
	ds_read_b128 v[166:169], v129 offset:45056
	ds_read_b128 v[242:245], v129 offset:47104
	v_add_u32_e32 v102, 0x6000, v94
	v_lshl_add_u64 v[8:9], v[198:199], 0, s[62:63]
	v_readfirstlane_b32 s92, v102
	s_mov_b32 m0, s92
	s_nop 0
	global_load_lds_dwordx4 v[8:9], off
	v_cvt_pk_f16_f32 v9, v68, v69
	v_cvt_pk_f16_f32 v8, v66, v67
	ds_write_b64 v100, v[8:9] offset:12288
	s_add_u32 s80, s22, 0x60400
	s_addc_u32 s81, s90, 0
	s_add_u32 s100, s22, 0x20400
	s_addc_u32 s101, s90, 0
	global_load_dwordx4 v[42:45], v201, s[100:101] nt
	s_setprio 1
	s_waitcnt lgkmcnt(1)
	v_mfma_f32_16x16x32_f16 v[66:69], v[166:169], v[226:229], v[210:213]
	v_mfma_f32_16x16x32_f16 v[210:213], v[166:169], v[230:233], v[214:217]
	v_mfma_f32_16x16x32_f16 v[214:217], v[166:169], v[234:237], v[218:221]
	v_mfma_f32_16x16x32_f16 v[166:169], v[166:169], v[238:241], v[190:193]
	v_mfma_f32_16x16x32_f16 v[190:193], v[242:245], v[226:229], v[202:205]
	v_mfma_f32_16x16x32_f16 v[202:205], v[242:245], v[230:233], v[206:209]
	v_mfma_f32_16x16x32_f16 v[206:209], v[242:245], v[234:237], v[222:225]
	v_mfma_f32_16x16x32_f16 v[218:221], v[242:245], v[238:241], v[78:81]
	s_setprio 0
	s_nop 0
	ds_read_b128 v[222:225], v128 offset:32768
	ds_read_b128 v[226:229], v128 offset:34816
	ds_read_b128 v[230:233], v128 offset:36864
	ds_read_b128 v[234:237], v128 offset:38912
	ds_read_b128 v[238:241], v130 offset:32768
	ds_read_b128 v[242:245], v130 offset:34816
	v_cvt_pk_f16_f32 v9, v64, v65
	v_cvt_pk_f16_f32 v8, v62, v63
	ds_write_b64 v100, v[8:9] offset:16384
	s_add_u32 s80, s22, 0x80400
	s_addc_u32 s81, s90, 0
	s_add_u32 s100, s22, 0x40400
	s_addc_u32 s101, s90, 0
	global_load_dwordx4 v[46:49], v201, s[100:101] nt
	s_setprio 1
	s_waitcnt lgkmcnt(1)
	v_mfma_f32_16x16x32_f16 v[62:65], v[238:241], v[222:225], v[70:73]
	v_mfma_f32_16x16x32_f16 v[70:73], v[238:241], v[226:229], v[90:93]
	v_mfma_f32_16x16x32_f16 v[104:107], v[238:241], v[230:233], v[104:107]
	v_mfma_f32_16x16x32_f16 v[108:111], v[242:245], v[222:225], v[108:111]
	v_mfma_f32_16x16x32_f16 v[112:115], v[242:245], v[226:229], v[112:115]
	v_mfma_f32_16x16x32_f16 v[116:119], v[242:245], v[230:233], v[116:119]
	v_mfma_f32_16x16x32_f16 v[238:241], v[238:241], v[234:237], v[82:85]
	v_mfma_f32_16x16x32_f16 v[242:245], v[242:245], v[234:237], v[86:89]
	s_setprio 0
	s_nop 1
	ds_read_b128 v[86:89], v130 offset:36864
	ds_read_b128 v[90:93], v130 offset:38912
	v_cvt_pk_f16_f32 v9, v60, v61
	v_cvt_pk_f16_f32 v8, v58, v59
	ds_write_b64 v100, v[8:9] offset:20480
	s_add_u32 s80, s22, 0xa0400
	s_addc_u32 s81, s90, 0
	s_add_u32 s100, s22, 0x60400
	s_addc_u32 s101, s90, 0
	global_load_dwordx4 v[74:77], v201, s[100:101] nt
	s_setprio 1
	s_waitcnt lgkmcnt(1)
	v_mfma_f32_16x16x32_f16 v[58:61], v[86:89], v[222:225], v[138:141]
	v_mfma_f32_16x16x32_f16 v[138:141], v[86:89], v[226:229], v[142:145]
	v_mfma_f32_16x16x32_f16 v[142:145], v[86:89], v[230:233], v[146:149]
	v_mfma_f32_16x16x32_f16 v[120:123], v[86:89], v[234:237], v[120:123]
	v_mfma_f32_16x16x32_f16 v[124:127], v[90:93], v[222:225], v[124:127]
	v_mfma_f32_16x16x32_f16 v[146:149], v[90:93], v[226:229], v[150:153]
	v_mfma_f32_16x16x32_f16 v[134:137], v[90:93], v[234:237], v[134:137]
	v_mfma_f32_16x16x32_f16 v[150:153], v[90:93], v[230:233], v[154:157]
	s_setprio 0
	ds_read_b128 v[90:93], v130 offset:40960
	s_nop 0
	ds_read_b128 v[154:157], v130 offset:43008
	v_cvt_pk_f16_f32 v9, v56, v57
	v_cvt_pk_f16_f32 v8, v54, v55
	ds_write_b64 v100, v[8:9] offset:24576
	s_add_u32 s80, s22, 0xc0400
	s_addc_u32 s81, s90, 0
	s_add_u32 s100, s22, 0x80400
	s_addc_u32 s101, s90, 0
	global_load_dwordx4 v[78:81], v201, s[100:101] nt
	s_add_u32 s100, s22, 0xa0400
	s_addc_u32 s101, s90, 0
	global_load_dwordx4 v[82:85], v201, s[100:101] nt
	s_setprio 1
	s_waitcnt lgkmcnt(1)
	v_mfma_f32_16x16x32_f16 v[246:249], v[90:93], v[222:225], v[4:7]
	v_mfma_f32_16x16x32_f16 v[170:173], v[90:93], v[226:229], v[170:173]
	v_mfma_f32_16x16x32_f16 v[174:177], v[90:93], v[230:233], v[174:177]
	v_mfma_f32_16x16x32_f16 v[162:165], v[90:93], v[234:237], v[162:165]
	v_mfma_f32_16x16x32_f16 v[178:181], v[154:157], v[222:225], v[178:181]
	v_mfma_f32_16x16x32_f16 v[182:185], v[154:157], v[226:229], v[182:185]
	v_mfma_f32_16x16x32_f16 v[186:189], v[154:157], v[230:233], v[186:189]
	v_mfma_f32_16x16x32_f16 v[154:157], v[154:157], v[234:237], v[158:161]
	s_setprio 0
	ds_read_b128 v[4:7], v130 offset:45056
	ds_read_b128 v[54:57], v130 offset:47104
	v_cvt_pk_f16_f32 v9, v52, v53
	v_cvt_pk_f16_f32 v8, v50, v51
	ds_write_b64 v100, v[8:9] offset:28672
	s_add_u32 s80, s22, 0xe0400
	s_addc_u32 s81, s90, 0
	s_add_u32 s100, s22, 0xc0400
	s_addc_u32 s101, s90, 0
	global_load_dwordx4 v[86:89], v201, s[100:101] nt
	s_add_u32 s100, s22, 0xe0400
	s_addc_u32 s101, s90, 0
	global_load_dwordx4 v[90:93], v201, s[100:101] nt
	s_setprio 1
	s_waitcnt lgkmcnt(1)
	v_mfma_f32_16x16x32_f16 v[66:69], v[4:7], v[222:225], v[66:69]
	v_mfma_f32_16x16x32_f16 v[158:161], v[4:7], v[226:229], v[210:213]
	v_mfma_f32_16x16x32_f16 v[210:213], v[4:7], v[230:233], v[214:217]
	v_mfma_f32_16x16x32_f16 v[166:169], v[4:7], v[234:237], v[166:169]
	v_mfma_f32_16x16x32_f16 v[190:193], v[54:57], v[222:225], v[190:193]
	v_mfma_f32_16x16x32_f16 v[202:205], v[54:57], v[226:229], v[202:205]
	v_mfma_f32_16x16x32_f16 v[206:209], v[54:57], v[230:233], v[206:209]
	v_mfma_f32_16x16x32_f16 v[214:217], v[54:57], v[234:237], v[218:221]
	s_setprio 0
	s_waitcnt vmcnt(7)
	s_waitcnt lgkmcnt(0)
	s_barrier
	s_nop 0
	ds_read_b128 v[218:221], v131
	ds_read_b128 v[222:225], v131 offset:2048
	ds_read_b128 v[226:229], v131 offset:4096
	ds_read_b128 v[230:233], v131 offset:6144
	ds_read_b128 v[50:53], v129
	ds_read_b128 v[54:57], v129 offset:2048
	s_add_u32 s80, s22, 0x500
	v_lshl_add_u64 v[8:9], s[30:31], 0, v[196:197]
	s_addc_u32 s81, s90, 0
	s_mov_b32 m0, s0
	v_cvt_pk_f16_f32 v5, v32, v33
	global_load_lds_dwordx4 v[8:9], off
	v_cvt_pk_f16_f32 v4, v30, v31
	ds_write_b64 v100, v[4:5] offset:32768
	s_setprio 1
	s_waitcnt lgkmcnt(1)
	v_mfma_f32_16x16x32_f16 v[30:33], v[50:53], v[218:221], v[62:65]
	v_mfma_f32_16x16x32_f16 v[70:73], v[50:53], v[222:225], v[70:73]
	v_mfma_f32_16x16x32_f16 v[104:107], v[50:53], v[226:229], v[104:107]
	v_mfma_f32_16x16x32_f16 v[108:111], v[54:57], v[218:221], v[108:111]
	v_mfma_f32_16x16x32_f16 v[112:115], v[54:57], v[222:225], v[112:115]
	v_mfma_f32_16x16x32_f16 v[116:119], v[54:57], v[226:229], v[116:119]
	v_mfma_f32_16x16x32_f16 v[234:237], v[50:53], v[230:233], v[238:241]
	v_mfma_f32_16x16x32_f16 v[238:241], v[54:57], v[230:233], v[242:245]
	s_setprio 0
	ds_read_b128 v[54:57], v129 offset:4096
	ds_read_b128 v[62:65], v129 offset:6144
	s_mov_b32 m0, s1
	v_lshl_add_u64 v[50:51], v[8:9], 0, s[58:59]
	global_load_lds_dwordx4 v[50:51], off
	v_cvt_pk_f16_f32 v29, v28, v29
	v_cvt_pk_f16_f32 v28, v26, v27
	ds_write_b64 v100, v[28:29] offset:36864
	s_add_u32 s0, s22, 0x20500
	s_addc_u32 s1, s90, 0
	s_setprio 1
	s_waitcnt lgkmcnt(1)
	v_mfma_f32_16x16x32_f16 v[26:29], v[54:57], v[218:221], v[58:61]
	v_mfma_f32_16x16x32_f16 v[120:123], v[54:57], v[230:233], v[120:123]
	v_mfma_f32_16x16x32_f16 v[124:127], v[62:65], v[218:221], v[124:127]
	v_mfma_f32_16x16x32_f16 v[146:149], v[62:65], v[222:225], v[146:149]
	v_mfma_f32_16x16x32_f16 v[134:137], v[62:65], v[230:233], v[134:137]
	v_mfma_f32_16x16x32_f16 v[138:141], v[54:57], v[222:225], v[138:141]
	v_mfma_f32_16x16x32_f16 v[142:145], v[54:57], v[226:229], v[142:145]
	v_mfma_f32_16x16x32_f16 v[150:153], v[62:65], v[226:229], v[150:153]
	s_setprio 0
	ds_read_b128 v[58:61], v129 offset:8192
	ds_read_b128 v[62:65], v129 offset:10240
	s_mov_b32 m0, s71
	v_lshl_add_u64 v[54:55], v[8:9], 0, s[60:61]
	global_load_lds_dwordx4 v[54:55], off
	v_cvt_pk_f16_f32 v25, v24, v25
	v_cvt_pk_f16_f32 v24, v22, v23
	ds_write_b64 v100, v[24:25] offset:40960
	s_add_u32 s0, s22, 0x40500
	s_addc_u32 s1, s90, 0
	s_add_u32 s100, s22, 0x500
	s_addc_u32 s101, s90, 0
	global_load_dwordx4 v[4:7], v201, s[100:101] nt
	s_setprio 1
	s_waitcnt lgkmcnt(1)
	v_mfma_f32_16x16x32_f16 v[22:25], v[58:61], v[218:221], v[246:249]
	v_mfma_f32_16x16x32_f16 v[170:173], v[58:61], v[222:225], v[170:173]
	v_mfma_f32_16x16x32_f16 v[174:177], v[58:61], v[226:229], v[174:177]
	v_mfma_f32_16x16x32_f16 v[162:165], v[58:61], v[230:233], v[162:165]
	v_mfma_f32_16x16x32_f16 v[178:181], v[62:65], v[218:221], v[178:181]
	v_mfma_f32_16x16x32_f16 v[182:185], v[62:65], v[222:225], v[182:185]
	v_mfma_f32_16x16x32_f16 v[186:189], v[62:65], v[226:229], v[186:189]
	v_mfma_f32_16x16x32_f16 v[154:157], v[62:65], v[230:233], v[154:157]
	s_setprio 0
	ds_read_b128 v[62:65], v129 offset:12288
	ds_read_b128 v[242:245], v129 offset:14336
	s_mov_b32 m0, s72
	v_lshl_add_u64 v[8:9], v[8:9], 0, s[62:63]
	global_load_lds_dwordx4 v[8:9], off
	v_cvt_pk_f16_f32 v9, v20, v21
	v_cvt_pk_f16_f32 v8, v18, v19
	ds_write_b64 v100, v[8:9] offset:45056
	s_add_u32 s0, s22, 0x60500
	s_addc_u32 s1, s90, 0
	s_add_u32 s100, s22, 0x20500
	s_addc_u32 s101, s90, 0
	global_load_dwordx4 v[50:53], v201, s[100:101] nt
	s_setprio 1
	s_waitcnt lgkmcnt(1)
	v_mfma_f32_16x16x32_f16 v[18:21], v[62:65], v[218:221], v[66:69]
	v_mfma_f32_16x16x32_f16 v[158:161], v[62:65], v[222:225], v[158:161]
	v_mfma_f32_16x16x32_f16 v[210:213], v[62:65], v[226:229], v[210:213]
	v_mfma_f32_16x16x32_f16 v[166:169], v[62:65], v[230:233], v[166:169]
	v_mfma_f32_16x16x32_f16 v[190:193], v[242:245], v[218:221], v[190:193]
	v_mfma_f32_16x16x32_f16 v[202:205], v[242:245], v[222:225], v[202:205]
	v_mfma_f32_16x16x32_f16 v[206:209], v[242:245], v[226:229], v[206:209]
	v_mfma_f32_16x16x32_f16 v[214:217], v[242:245], v[230:233], v[214:217]
	s_setprio 0
	ds_read_b128 v[218:221], v128
	ds_read_b128 v[222:225], v128 offset:2048
	ds_read_b128 v[226:229], v128 offset:4096
	ds_read_b128 v[230:233], v128 offset:6144
	ds_read_b128 v[66:69], v130
	ds_read_b128 v[242:245], v130 offset:2048
	v_cvt_pk_f16_f32 v9, v16, v17
	v_cvt_pk_f16_f32 v8, v14, v15
	ds_write_b64 v100, v[8:9] offset:49152
	s_add_u32 s0, s22, 0x80500
	s_addc_u32 s1, s90, 0
	s_add_u32 s100, s22, 0x40500
	s_addc_u32 s101, s90, 0
	global_load_dwordx4 v[54:57], v201, s[100:101] nt
	s_setprio 1
	s_waitcnt lgkmcnt(1)
	v_mfma_f32_16x16x32_f16 v[14:17], v[66:69], v[218:221], v[30:33]
	v_mfma_f32_16x16x32_f16 v[30:33], v[66:69], v[222:225], v[70:73]
	v_mfma_f32_16x16x32_f16 v[104:107], v[66:69], v[226:229], v[104:107]
	v_mfma_f32_16x16x32_f16 v[108:111], v[242:245], v[218:221], v[108:111]
	v_mfma_f32_16x16x32_f16 v[112:115], v[242:245], v[222:225], v[112:115]
	v_mfma_f32_16x16x32_f16 v[116:119], v[242:245], v[226:229], v[116:119]
	v_mfma_f32_16x16x32_f16 v[234:237], v[66:69], v[230:233], v[234:237]
	v_mfma_f32_16x16x32_f16 v[238:241], v[242:245], v[230:233], v[238:241]
	s_setprio 0
	ds_read_b128 v[70:73], v130 offset:4096
	ds_read_b128 v[242:245], v130 offset:6144
	v_cvt_pk_f16_f32 v9, v12, v13
	v_cvt_pk_f16_f32 v8, v10, v11
	ds_write_b64 v100, v[8:9] offset:53248
	s_add_u32 s0, s22, 0xa0500
	s_addc_u32 s1, s90, 0
	s_add_u32 s100, s22, 0x60500
	s_addc_u32 s101, s90, 0
	global_load_dwordx4 v[58:61], v201, s[100:101] nt
	s_setprio 1
	s_waitcnt lgkmcnt(1)
	v_mfma_f32_16x16x32_f16 v[26:29], v[70:73], v[218:221], v[26:29]
	v_mfma_f32_16x16x32_f16 v[120:123], v[70:73], v[230:233], v[120:123]
	v_mfma_f32_16x16x32_f16 v[124:127], v[242:245], v[218:221], v[124:127]
	v_mfma_f32_16x16x32_f16 v[146:149], v[242:245], v[222:225], v[146:149]
	v_mfma_f32_16x16x32_f16 v[134:137], v[242:245], v[230:233], v[134:137]
	v_mfma_f32_16x16x32_f16 v[138:141], v[70:73], v[222:225], v[138:141]
	v_mfma_f32_16x16x32_f16 v[142:145], v[70:73], v[226:229], v[142:145]
	v_mfma_f32_16x16x32_f16 v[150:153], v[242:245], v[226:229], v[150:153]
	s_setprio 0
	ds_read_b128 v[8:11], v130 offset:8192
	ds_read_b128 v[242:245], v130 offset:10240
	v_cvt_pk_f16_f32 v13, v36, v37
	v_cvt_pk_f16_f32 v12, v34, v35
	ds_write_b64 v100, v[12:13] offset:57344
	s_add_u32 s0, s22, 0xc0500
	s_addc_u32 s1, s90, 0
	s_add_u32 s100, s22, 0x80500
	s_addc_u32 s101, s90, 0
	global_load_dwordx4 v[62:65], v201, s[100:101] nt
	s_add_u32 s100, s22, 0xa0500
	s_addc_u32 s101, s90, 0
	global_load_dwordx4 v[66:69], v201, s[100:101] nt
	s_setprio 1
	s_waitcnt lgkmcnt(1)
	v_mfma_f32_16x16x32_f16 v[22:25], v[8:11], v[218:221], v[22:25]
	v_mfma_f32_16x16x32_f16 v[170:173], v[8:11], v[222:225], v[170:173]
	v_mfma_f32_16x16x32_f16 v[174:177], v[8:11], v[226:229], v[174:177]
	v_mfma_f32_16x16x32_f16 v[162:165], v[8:11], v[230:233], v[162:165]
	v_mfma_f32_16x16x32_f16 v[178:181], v[242:245], v[218:221], v[178:181]
	v_mfma_f32_16x16x32_f16 v[182:185], v[242:245], v[222:225], v[182:185]
	v_mfma_f32_16x16x32_f16 v[186:189], v[242:245], v[226:229], v[186:189]
	v_mfma_f32_16x16x32_f16 v[154:157], v[242:245], v[230:233], v[154:157]
	s_setprio 0
	ds_read_b128 v[8:11], v130 offset:12288
	ds_read_b128 v[242:245], v130 offset:14336
	v_cvt_pk_f16_f32 v13, v40, v41
	v_cvt_pk_f16_f32 v12, v38, v39
	ds_write_b64 v100, v[12:13] offset:61440
	s_add_u32 s0, s22, 0xe0500
	s_addc_u32 s1, s90, 0
	s_add_u32 s100, s22, 0xc0500
	s_addc_u32 s101, s90, 0
	global_load_dwordx4 v[70:73], v201, s[100:101] nt
	s_add_u32 s100, s22, 0xe0500
	s_addc_u32 s101, s90, 0
	global_load_dwordx4 v[36:39], v201, s[100:101] nt
	s_setprio 1
	s_waitcnt lgkmcnt(1)
	v_mfma_f32_16x16x32_f16 v[246:249], v[8:11], v[218:221], v[18:21]
	v_mfma_f32_16x16x32_f16 v[158:161], v[8:11], v[222:225], v[158:161]
	v_mfma_f32_16x16x32_f16 v[210:213], v[8:11], v[226:229], v[210:213]
	v_mfma_f32_16x16x32_f16 v[166:169], v[8:11], v[230:233], v[166:169]
	v_mfma_f32_16x16x32_f16 v[190:193], v[242:245], v[218:221], v[190:193]
	v_mfma_f32_16x16x32_f16 v[202:205], v[242:245], v[222:225], v[202:205]
	v_mfma_f32_16x16x32_f16 v[206:209], v[242:245], v[226:229], v[206:209]
	v_mfma_f32_16x16x32_f16 v[214:217], v[242:245], v[230:233], v[214:217]
	s_setprio 0
	s_waitcnt vmcnt(7)
	s_waitcnt lgkmcnt(0)
	s_barrier
	ds_read_b128 v[218:221], v131 offset:32768
	ds_read_b128 v[222:225], v131 offset:34816
	ds_read_b128 v[226:229], v131 offset:36864
	ds_read_b128 v[230:233], v131 offset:38912
	ds_read_b128 v[8:11], v129 offset:32768
	ds_read_b128 v[18:21], v129 offset:34816
	s_add_u32 s0, s22, 0x600
	s_addc_u32 s1, s90, 0
	v_lshl_add_u64 v[34:35], s[34:35], 0, v[196:197]
	s_mov_b32 m0, s70
	v_cvt_pk_f16_f32 v3, v2, v3
	global_load_lds_dwordx4 v[34:35], off
	v_cvt_pk_f16_f32 v2, v0, v1
	ds_write_b64 v100, v[2:3]
	s_setprio 1
	s_waitcnt lgkmcnt(1)
	v_mfma_f32_16x16x32_f16 v[30:33], v[8:11], v[222:225], v[30:33]
	v_mfma_f32_16x16x32_f16 v[104:107], v[8:11], v[226:229], v[104:107]
	v_mfma_f32_16x16x32_f16 v[108:111], v[18:21], v[218:221], v[108:111]
	v_mfma_f32_16x16x32_f16 v[112:115], v[18:21], v[222:225], v[112:115]
	v_mfma_f32_16x16x32_f16 v[116:119], v[18:21], v[226:229], v[116:119]
	v_mfma_f32_16x16x32_f16 v[242:245], v[8:11], v[218:221], v[14:17]
	v_mfma_f32_16x16x32_f16 v[234:237], v[8:11], v[230:233], v[234:237]
	v_mfma_f32_16x16x32_f16 v[238:241], v[18:21], v[230:233], v[238:241]
	s_setprio 0
	ds_read_b128 v[12:15], v129 offset:36864
	ds_read_b128 v[16:19], v129 offset:38912
	s_mov_b32 m0, s73
	v_lshl_add_u64 v[8:9], v[34:35], 0, s[58:59]
	global_load_lds_dwordx4 v[8:9], off
	v_cvt_pk_f16_f32 v9, v44, v45
	v_cvt_pk_f16_f32 v8, v42, v43
	ds_write_b64 v100, v[8:9] offset:4096
	s_add_u32 s0, s22, 0x20600
	s_addc_u32 s1, s90, 0
	s_setprio 1
	s_waitcnt lgkmcnt(1)
	v_mfma_f32_16x16x32_f16 v[40:43], v[12:15], v[218:221], v[26:29]
	v_mfma_f32_16x16x32_f16 v[120:123], v[12:15], v[230:233], v[120:123]
	v_mfma_f32_16x16x32_f16 v[124:127], v[16:19], v[218:221], v[124:127]
	v_mfma_f32_16x16x32_f16 v[146:149], v[16:19], v[222:225], v[146:149]
	v_mfma_f32_16x16x32_f16 v[134:137], v[16:19], v[230:233], v[134:137]
	v_mfma_f32_16x16x32_f16 v[138:141], v[12:15], v[222:225], v[138:141]
	v_mfma_f32_16x16x32_f16 v[142:145], v[12:15], v[226:229], v[142:145]
	v_mfma_f32_16x16x32_f16 v[150:153], v[16:19], v[226:229], v[150:153]
	s_setprio 0
	ds_read_b128 v[16:19], v129 offset:40960
	ds_read_b128 v[26:29], v129 offset:43008
	s_mov_b32 m0, s91
	v_lshl_add_u64 v[12:13], v[34:35], 0, s[60:61]
	global_load_lds_dwordx4 v[12:13], off
	v_cvt_pk_f16_f32 v13, v48, v49
	v_cvt_pk_f16_f32 v12, v46, v47
	ds_write_b64 v100, v[12:13] offset:8192
	s_add_u32 s0, s22, 0x40600
	s_addc_u32 s1, s90, 0
	s_add_u32 s100, s22, 0x600
	s_addc_u32 s101, s90, 0
	global_load_dwordx4 v[0:3], v201, s[100:101] nt
	s_setprio 1
	s_waitcnt lgkmcnt(1)
	v_mfma_f32_16x16x32_f16 v[44:47], v[16:19], v[218:221], v[22:25]
	v_mfma_f32_16x16x32_f16 v[170:173], v[16:19], v[222:225], v[170:173]
	v_mfma_f32_16x16x32_f16 v[174:177], v[16:19], v[226:229], v[174:177]
	v_mfma_f32_16x16x32_f16 v[162:165], v[16:19], v[230:233], v[162:165]
	v_mfma_f32_16x16x32_f16 v[178:181], v[26:29], v[218:221], v[178:181]
	v_mfma_f32_16x16x32_f16 v[182:185], v[26:29], v[222:225], v[182:185]
	v_mfma_f32_16x16x32_f16 v[186:189], v[26:29], v[226:229], v[186:189]
	v_mfma_f32_16x16x32_f16 v[154:157], v[26:29], v[230:233], v[154:157]
	s_setprio 0
	ds_read_b128 v[20:23], v129 offset:45056
	ds_read_b128 v[24:27], v129 offset:47104
	s_mov_b32 m0, s92
	v_lshl_add_u64 v[16:17], v[34:35], 0, s[62:63]
	global_load_lds_dwordx4 v[16:17], off
	v_cvt_pk_f16_f32 v17, v76, v77
	v_cvt_pk_f16_f32 v16, v74, v75
	ds_write_b64 v100, v[16:17] offset:12288
	s_add_u32 s0, s22, 0x60600
	s_addc_u32 s1, s90, 0
	s_add_u32 s100, s22, 0x20600
	s_addc_u32 s101, s90, 0
	global_load_dwordx4 v[8:11], v201, s[100:101] nt
	s_setprio 1
	s_waitcnt lgkmcnt(1)
	v_mfma_f32_16x16x32_f16 v[74:77], v[20:23], v[218:221], v[246:249]
	v_mfma_f32_16x16x32_f16 v[158:161], v[20:23], v[222:225], v[158:161]
	v_mfma_f32_16x16x32_f16 v[210:213], v[20:23], v[226:229], v[210:213]
	v_mfma_f32_16x16x32_f16 v[166:169], v[20:23], v[230:233], v[166:169]
	v_mfma_f32_16x16x32_f16 v[190:193], v[24:27], v[218:221], v[190:193]
	v_mfma_f32_16x16x32_f16 v[202:205], v[24:27], v[222:225], v[202:205]
	v_mfma_f32_16x16x32_f16 v[206:209], v[24:27], v[226:229], v[206:209]
	v_mfma_f32_16x16x32_f16 v[214:217], v[24:27], v[230:233], v[214:217]
	s_setprio 0
	ds_read_b128 v[218:221], v128 offset:32768
	ds_read_b128 v[222:225], v128 offset:34816
	ds_read_b128 v[226:229], v128 offset:36864
	ds_read_b128 v[230:233], v128 offset:38912
	ds_read_b128 v[24:27], v130 offset:32768
	ds_read_b128 v[246:249], v130 offset:34816
	v_cvt_pk_f16_f32 v21, v80, v81
	v_cvt_pk_f16_f32 v20, v78, v79
	ds_write_b64 v100, v[20:21] offset:16384
	s_add_u32 s0, s22, 0x80600
	s_addc_u32 s1, s90, 0
	s_add_u32 s100, s22, 0x40600
	s_addc_u32 s101, s90, 0
	global_load_dwordx4 v[12:15], v201, s[100:101] nt
	s_setprio 1
	s_waitcnt lgkmcnt(1)
	v_mfma_f32_16x16x32_f16 v[78:81], v[24:27], v[218:221], v[242:245]
	v_mfma_f32_16x16x32_f16 v[104:107], v[24:27], v[226:229], v[104:107]
	v_mfma_f32_16x16x32_f16 v[108:111], v[246:249], v[218:221], v[108:111]
	v_mfma_f32_16x16x32_f16 v[112:115], v[246:249], v[222:225], v[112:115]
	v_mfma_f32_16x16x32_f16 v[116:119], v[246:249], v[226:229], v[116:119]
	v_mfma_f32_16x16x32_f16 v[242:245], v[24:27], v[222:225], v[30:33]
	v_mfma_f32_16x16x32_f16 v[234:237], v[24:27], v[230:233], v[234:237]
	v_mfma_f32_16x16x32_f16 v[238:241], v[246:249], v[230:233], v[238:241]
	s_setprio 0
	ds_read_b128 v[28:31], v130 offset:36864
	ds_read_b128 v[32:35], v130 offset:38912
	v_cvt_pk_f16_f32 v25, v84, v85
	v_cvt_pk_f16_f32 v24, v82, v83
	ds_write_b64 v100, v[24:25] offset:20480
	s_add_u32 s0, s22, 0xa0600
	s_addc_u32 s1, s90, 0
	s_add_u32 s100, s22, 0x60600
	s_addc_u32 s101, s90, 0
	global_load_dwordx4 v[16:19], v201, s[100:101] nt
	s_setprio 1
	s_waitcnt lgkmcnt(1)
	v_mfma_f32_16x16x32_f16 v[82:85], v[28:31], v[218:221], v[40:43]
	v_mfma_f32_16x16x32_f16 v[120:123], v[28:31], v[230:233], v[120:123]
	v_mfma_f32_16x16x32_f16 v[124:127], v[32:35], v[218:221], v[124:127]
	v_mfma_f32_16x16x32_f16 v[146:149], v[32:35], v[222:225], v[146:149]
	v_mfma_f32_16x16x32_f16 v[134:137], v[32:35], v[230:233], v[134:137]
	v_mfma_f32_16x16x32_f16 v[138:141], v[28:31], v[222:225], v[138:141]
	v_mfma_f32_16x16x32_f16 v[142:145], v[28:31], v[226:229], v[142:145]
	v_mfma_f32_16x16x32_f16 v[150:153], v[32:35], v[226:229], v[150:153]
	s_setprio 0
	ds_read_b128 v[32:35], v130 offset:40960
	ds_read_b128 v[40:43], v130 offset:43008
	v_cvt_pk_f16_f32 v29, v88, v89
	v_cvt_pk_f16_f32 v28, v86, v87
	ds_write_b64 v100, v[28:29] offset:24576
	s_add_u32 s0, s22, 0xc0600
	s_addc_u32 s1, s90, 0
	s_add_u32 s100, s22, 0x80600
	s_addc_u32 s101, s90, 0
	global_load_dwordx4 v[20:23], v201, s[100:101] nt
	s_add_u32 s100, s22, 0xa0600
	s_addc_u32 s101, s90, 0
	global_load_dwordx4 v[24:27], v201, s[100:101] nt
	s_setprio 1
	s_waitcnt lgkmcnt(1)
	v_mfma_f32_16x16x32_f16 v[86:89], v[32:35], v[218:221], v[44:47]
	v_mfma_f32_16x16x32_f16 v[170:173], v[32:35], v[222:225], v[170:173]
	v_mfma_f32_16x16x32_f16 v[174:177], v[32:35], v[226:229], v[174:177]
	v_mfma_f32_16x16x32_f16 v[162:165], v[32:35], v[230:233], v[162:165]
	v_mfma_f32_16x16x32_f16 v[178:181], v[40:43], v[218:221], v[178:181]
	v_mfma_f32_16x16x32_f16 v[182:185], v[40:43], v[222:225], v[182:185]
	v_mfma_f32_16x16x32_f16 v[186:189], v[40:43], v[226:229], v[186:189]
	v_mfma_f32_16x16x32_f16 v[154:157], v[40:43], v[230:233], v[154:157]
	s_setprio 0
	ds_read_b128 v[40:43], v130 offset:45056
	ds_read_b128 v[44:47], v130 offset:47104
	v_cvt_pk_f16_f32 v33, v92, v93
	v_cvt_pk_f16_f32 v32, v90, v91
	ds_write_b64 v100, v[32:33] offset:28672
	s_add_u32 s0, s22, 0xe0600
	s_addc_u32 s1, s90, 0
	s_add_u32 s100, s22, 0xc0600
	s_addc_u32 s101, s90, 0
	global_load_dwordx4 v[28:31], v201, s[100:101] nt
	s_add_u32 s100, s22, 0xe0600
	s_addc_u32 s101, s90, 0
	global_load_dwordx4 v[32:35], v201, s[100:101] nt
	s_setprio 1
	s_waitcnt lgkmcnt(1)
	v_mfma_f32_16x16x32_f16 v[74:77], v[40:43], v[218:221], v[74:77]
	v_mfma_f32_16x16x32_f16 v[90:93], v[40:43], v[222:225], v[158:161]
	v_mfma_f32_16x16x32_f16 v[158:161], v[40:43], v[226:229], v[210:213]
	v_mfma_f32_16x16x32_f16 v[166:169], v[40:43], v[230:233], v[166:169]
	v_mfma_f32_16x16x32_f16 v[190:193], v[44:47], v[218:221], v[190:193]
	v_mfma_f32_16x16x32_f16 v[202:205], v[44:47], v[222:225], v[202:205]
	v_mfma_f32_16x16x32_f16 v[206:209], v[44:47], v[226:229], v[206:209]
	v_mfma_f32_16x16x32_f16 v[210:213], v[44:47], v[230:233], v[214:217]
	s_setprio 0
	s_waitcnt vmcnt(7)
	s_waitcnt lgkmcnt(0)
	s_barrier
	s_nop 0
	ds_read_b128 v[214:217], v131
	ds_read_b128 v[218:221], v131 offset:2048
	ds_read_b128 v[222:225], v131 offset:4096
	ds_read_b128 v[226:229], v131 offset:6144
	ds_read_b128 v[40:43], v129
	ds_read_b128 v[44:47], v129 offset:2048
	s_add_u32 s70, s22, 0x700
	s_addc_u32 s71, s90, 0
	v_lshl_add_u64 v[198:199], s[36:37], 0, v[196:197]
	v_readfirstlane_b32 s0, v95
	s_mov_b32 m0, s0
	v_cvt_pk_f16_f32 v7, v6, v7
	global_load_lds_dwordx4 v[198:199], off
	v_cvt_pk_f16_f32 v6, v4, v5
	ds_write_b64 v100, v[6:7] offset:32768
	s_setprio 1
	s_waitcnt lgkmcnt(1)
	v_mfma_f32_16x16x32_f16 v[78:81], v[40:43], v[214:217], v[78:81]
	v_mfma_f32_16x16x32_f16 v[104:107], v[40:43], v[222:225], v[104:107]
	v_mfma_f32_16x16x32_f16 v[108:111], v[44:47], v[214:217], v[108:111]
	v_mfma_f32_16x16x32_f16 v[112:115], v[44:47], v[218:221], v[112:115]
	v_mfma_f32_16x16x32_f16 v[116:119], v[44:47], v[222:225], v[116:119]
	v_mfma_f32_16x16x32_f16 v[230:233], v[40:43], v[218:221], v[242:245]
	v_mfma_f32_16x16x32_f16 v[234:237], v[40:43], v[226:229], v[234:237]
	v_mfma_f32_16x16x32_f16 v[238:241], v[44:47], v[226:229], v[238:241]
	s_setprio 0
	ds_read_b128 v[44:47], v129 offset:4096
	ds_read_b128 v[242:245], v129 offset:6144
	v_readfirstlane_b32 s72, v96
	v_lshl_add_u64 v[40:41], v[198:199], 0, s[58:59]
	s_mov_b32 m0, s72
	s_nop 0
	global_load_lds_dwordx4 v[40:41], off
	v_cvt_pk_f16_f32 v41, v52, v53
	v_cvt_pk_f16_f32 v40, v50, v51
	ds_write_b64 v100, v[40:41] offset:36864
	s_add_u32 s70, s22, 0x20700
	s_addc_u32 s71, s90, 0
	s_setprio 1
	s_waitcnt lgkmcnt(1)
	v_mfma_f32_16x16x32_f16 v[82:85], v[44:47], v[214:217], v[82:85]
	v_mfma_f32_16x16x32_f16 v[120:123], v[44:47], v[226:229], v[120:123]
	v_mfma_f32_16x16x32_f16 v[124:127], v[242:245], v[214:217], v[124:127]
	v_mfma_f32_16x16x32_f16 v[146:149], v[242:245], v[218:221], v[146:149]
	v_mfma_f32_16x16x32_f16 v[134:137], v[242:245], v[226:229], v[134:137]
	v_mfma_f32_16x16x32_f16 v[138:141], v[44:47], v[218:221], v[138:141]
	v_mfma_f32_16x16x32_f16 v[142:145], v[44:47], v[222:225], v[142:145]
	v_mfma_f32_16x16x32_f16 v[150:153], v[242:245], v[222:225], v[150:153]
	s_setprio 0
	ds_read_b128 v[48:51], v129 offset:8192
	ds_read_b128 v[242:245], v129 offset:10240
	v_readfirstlane_b32 s71, v97
	v_lshl_add_u64 v[44:45], v[198:199], 0, s[60:61]
	s_mov_b32 m0, s71
	s_nop 0
	global_load_lds_dwordx4 v[44:45], off
	v_cvt_pk_f16_f32 v45, v56, v57
	v_cvt_pk_f16_f32 v44, v54, v55
	ds_write_b64 v100, v[44:45] offset:40960
	s_add_u32 s80, s22, 0x40700
	s_addc_u32 s81, s90, 0
	s_add_u32 s100, s22, 0x700
	s_addc_u32 s101, s90, 0
	global_load_dwordx4 v[4:7], v201, s[100:101] nt
	s_setprio 1
	s_waitcnt lgkmcnt(1)
	v_mfma_f32_16x16x32_f16 v[86:89], v[48:51], v[214:217], v[86:89]
	v_mfma_f32_16x16x32_f16 v[170:173], v[48:51], v[218:221], v[170:173]
	v_mfma_f32_16x16x32_f16 v[174:177], v[48:51], v[222:225], v[174:177]
	v_mfma_f32_16x16x32_f16 v[162:165], v[48:51], v[226:229], v[162:165]
	v_mfma_f32_16x16x32_f16 v[178:181], v[242:245], v[214:217], v[178:181]
	v_mfma_f32_16x16x32_f16 v[182:185], v[242:245], v[218:221], v[182:185]
	v_mfma_f32_16x16x32_f16 v[186:189], v[242:245], v[222:225], v[186:189]
	v_mfma_f32_16x16x32_f16 v[154:157], v[242:245], v[226:229], v[154:157]
	s_setprio 0
	ds_read_b128 v[52:55], v129 offset:12288
	ds_read_b128 v[242:245], v129 offset:14336
	v_readfirstlane_b32 s70, v98
	v_lshl_add_u64 v[48:49], v[198:199], 0, s[62:63]
	s_mov_b32 m0, s70
	s_nop 0
	global_load_lds_dwordx4 v[48:49], off
	v_cvt_pk_f16_f32 v49, v60, v61
	v_cvt_pk_f16_f32 v48, v58, v59
	ds_write_b64 v100, v[48:49] offset:45056
	s_add_u32 s80, s22, 0x60700
	s_addc_u32 s81, s90, 0
	s_add_u32 s100, s22, 0x20700
	s_addc_u32 s101, s90, 0
	global_load_dwordx4 v[40:43], v201, s[100:101] nt
	s_setprio 1
	s_waitcnt lgkmcnt(1)
	v_mfma_f32_16x16x32_f16 v[74:77], v[52:55], v[214:217], v[74:77]
	v_mfma_f32_16x16x32_f16 v[90:93], v[52:55], v[218:221], v[90:93]
	v_mfma_f32_16x16x32_f16 v[158:161], v[52:55], v[222:225], v[158:161]
	v_mfma_f32_16x16x32_f16 v[166:169], v[52:55], v[226:229], v[166:169]
	v_mfma_f32_16x16x32_f16 v[190:193], v[242:245], v[214:217], v[190:193]
	v_mfma_f32_16x16x32_f16 v[202:205], v[242:245], v[218:221], v[202:205]
	v_mfma_f32_16x16x32_f16 v[206:209], v[242:245], v[222:225], v[206:209]
	v_mfma_f32_16x16x32_f16 v[210:213], v[242:245], v[226:229], v[210:213]
	s_setprio 0
	ds_read_b128 v[214:217], v128
	ds_read_b128 v[218:221], v128 offset:2048
	ds_read_b128 v[222:225], v128 offset:4096
	ds_read_b128 v[226:229], v128 offset:6144
	ds_read_b128 v[56:59], v130
	ds_read_b128 v[242:245], v130 offset:2048
	v_cvt_pk_f16_f32 v53, v64, v65
	v_cvt_pk_f16_f32 v52, v62, v63
	ds_write_b64 v100, v[52:53] offset:49152
	s_add_u32 s80, s22, 0x80700
	s_addc_u32 s81, s90, 0
	s_add_u32 s100, s22, 0x40700
	s_addc_u32 s101, s90, 0
	global_load_dwordx4 v[44:47], v201, s[100:101] nt
	s_setprio 1
	s_waitcnt lgkmcnt(1)
	v_mfma_f32_16x16x32_f16 v[78:81], v[56:59], v[214:217], v[78:81]
	v_mfma_f32_16x16x32_f16 v[104:107], v[56:59], v[222:225], v[104:107]
	v_mfma_f32_16x16x32_f16 v[108:111], v[242:245], v[214:217], v[108:111]
	v_mfma_f32_16x16x32_f16 v[112:115], v[242:245], v[218:221], v[112:115]
	v_mfma_f32_16x16x32_f16 v[116:119], v[242:245], v[222:225], v[116:119]
	v_mfma_f32_16x16x32_f16 v[230:233], v[56:59], v[218:221], v[230:233]
	v_mfma_f32_16x16x32_f16 v[234:237], v[56:59], v[226:229], v[234:237]
	v_mfma_f32_16x16x32_f16 v[238:241], v[242:245], v[226:229], v[238:241]
	s_setprio 0
	ds_read_b128 v[60:63], v130 offset:4096
	ds_read_b128 v[242:245], v130 offset:6144
	v_cvt_pk_f16_f32 v57, v68, v69
	v_cvt_pk_f16_f32 v56, v66, v67
	ds_write_b64 v100, v[56:57] offset:53248
	s_add_u32 s80, s22, 0xa0700
	s_addc_u32 s81, s90, 0
	s_add_u32 s100, s22, 0x60700
	s_addc_u32 s101, s90, 0
	global_load_dwordx4 v[48:51], v201, s[100:101] nt
	s_setprio 1
	s_waitcnt lgkmcnt(1)
	v_mfma_f32_16x16x32_f16 v[82:85], v[60:63], v[214:217], v[82:85]
	v_mfma_f32_16x16x32_f16 v[120:123], v[60:63], v[226:229], v[120:123]
	v_mfma_f32_16x16x32_f16 v[124:127], v[242:245], v[214:217], v[124:127]
	v_mfma_f32_16x16x32_f16 v[146:149], v[242:245], v[218:221], v[146:149]
	v_mfma_f32_16x16x32_f16 v[134:137], v[242:245], v[226:229], v[134:137]
	v_mfma_f32_16x16x32_f16 v[138:141], v[60:63], v[218:221], v[138:141]
	v_mfma_f32_16x16x32_f16 v[142:145], v[60:63], v[222:225], v[142:145]
	v_mfma_f32_16x16x32_f16 v[150:153], v[242:245], v[222:225], v[150:153]
	s_setprio 0
	ds_read_b128 v[64:67], v130 offset:8192
	ds_read_b128 v[242:245], v130 offset:10240
	v_cvt_pk_f16_f32 v61, v72, v73
	v_cvt_pk_f16_f32 v60, v70, v71
	ds_write_b64 v100, v[60:61] offset:57344
	s_add_u32 s80, s22, 0xc0700
	s_addc_u32 s81, s90, 0
	s_add_u32 s100, s22, 0x80700
	s_addc_u32 s101, s90, 0
	global_load_dwordx4 v[52:55], v201, s[100:101] nt
	s_add_u32 s100, s22, 0xa0700
	s_addc_u32 s101, s90, 0
	global_load_dwordx4 v[56:59], v201, s[100:101] nt
	s_setprio 1
	s_waitcnt lgkmcnt(1)
	v_mfma_f32_16x16x32_f16 v[86:89], v[64:67], v[214:217], v[86:89]
	v_mfma_f32_16x16x32_f16 v[170:173], v[64:67], v[218:221], v[170:173]
	v_mfma_f32_16x16x32_f16 v[174:177], v[64:67], v[222:225], v[174:177]
	v_mfma_f32_16x16x32_f16 v[162:165], v[64:67], v[226:229], v[162:165]
	v_mfma_f32_16x16x32_f16 v[178:181], v[242:245], v[214:217], v[178:181]
	v_mfma_f32_16x16x32_f16 v[182:185], v[242:245], v[218:221], v[182:185]
	v_mfma_f32_16x16x32_f16 v[186:189], v[242:245], v[222:225], v[186:189]
	v_mfma_f32_16x16x32_f16 v[154:157], v[242:245], v[226:229], v[154:157]
	s_setprio 0
	ds_read_b128 v[64:67], v130 offset:12288
	ds_read_b128 v[68:71], v130 offset:14336
	v_cvt_pk_f16_f32 v39, v38, v39
	v_cvt_pk_f16_f32 v38, v36, v37
	ds_write_b64 v100, v[38:39] offset:61440
	s_add_u32 s80, s22, 0xe0700
	s_addc_u32 s81, s90, 0
	s_add_u32 s100, s22, 0xc0700
	s_addc_u32 s101, s90, 0
	global_load_dwordx4 v[60:63], v201, s[100:101] nt
	s_add_u32 s100, s22, 0xe0700
	s_addc_u32 s101, s90, 0
	global_load_dwordx4 v[36:39], v201, s[100:101] nt
	s_setprio 1
	s_waitcnt lgkmcnt(1)
	v_mfma_f32_16x16x32_f16 v[90:93], v[64:67], v[218:221], v[90:93]
	v_mfma_f32_16x16x32_f16 v[242:245], v[64:67], v[214:217], v[74:77]
	v_mfma_f32_16x16x32_f16 v[158:161], v[64:67], v[222:225], v[158:161]
	v_mfma_f32_16x16x32_f16 v[166:169], v[64:67], v[226:229], v[166:169]
	v_mfma_f32_16x16x32_f16 v[190:193], v[68:71], v[214:217], v[190:193]
	v_mfma_f32_16x16x32_f16 v[202:205], v[68:71], v[218:221], v[202:205]
	v_mfma_f32_16x16x32_f16 v[206:209], v[68:71], v[222:225], v[206:209]
	v_mfma_f32_16x16x32_f16 v[210:213], v[68:71], v[226:229], v[210:213]
	s_setprio 0
	s_waitcnt vmcnt(7)
	s_waitcnt lgkmcnt(0)
	s_barrier
	ds_read_b128 v[214:217], v131 offset:32768
	ds_read_b128 v[218:221], v131 offset:34816
	ds_read_b128 v[222:225], v131 offset:36864
	ds_read_b128 v[226:229], v131 offset:38912
	ds_read_b128 v[64:67], v129 offset:32768
	ds_read_b128 v[68:71], v129 offset:34816
	s_add_u32 s80, s22, 0x800
	s_addc_u32 s81, s90, 0
	v_lshl_add_u64 v[198:199], s[38:39], 0, v[196:197]
	v_readfirstlane_b32 s1, v94
	s_mov_b32 m0, s1
	v_cvt_pk_f16_f32 v3, v2, v3
	global_load_lds_dwordx4 v[198:199], off
	v_cvt_pk_f16_f32 v2, v0, v1
	ds_write_b64 v100, v[2:3]
	s_setprio 1
	s_waitcnt lgkmcnt(1)
	v_mfma_f32_16x16x32_f16 v[104:107], v[64:67], v[222:225], v[104:107]
	v_mfma_f32_16x16x32_f16 v[108:111], v[68:71], v[214:217], v[108:111]
	v_mfma_f32_16x16x32_f16 v[112:115], v[68:71], v[218:221], v[112:115]
	v_mfma_f32_16x16x32_f16 v[116:119], v[68:71], v[222:225], v[116:119]
	v_mfma_f32_16x16x32_f16 v[246:249], v[64:67], v[214:217], v[78:81]
	v_mfma_f32_16x16x32_f16 v[230:233], v[64:67], v[218:221], v[230:233]
	v_mfma_f32_16x16x32_f16 v[234:237], v[64:67], v[226:229], v[234:237]
	v_mfma_f32_16x16x32_f16 v[238:241], v[68:71], v[226:229], v[238:241]
	s_setprio 0
	ds_read_b128 v[68:71], v129 offset:36864
	ds_read_b128 v[72:75], v129 offset:38912
	v_readfirstlane_b32 s92, v99
	v_lshl_add_u64 v[64:65], v[198:199], 0, s[58:59]
	s_mov_b32 m0, s92
	v_cvt_pk_f16_f32 v11, v10, v11
	global_load_lds_dwordx4 v[64:65], off
	v_cvt_pk_f16_f32 v10, v8, v9
	ds_write_b64 v100, v[10:11] offset:4096
	s_add_u32 s80, s22, 0x20800
	s_addc_u32 s81, s90, 0
	s_setprio 1
	s_waitcnt lgkmcnt(1)
	v_mfma_f32_16x16x32_f16 v[8:11], v[68:71], v[214:217], v[82:85]
	v_mfma_f32_16x16x32_f16 v[120:123], v[68:71], v[226:229], v[120:123]
	v_mfma_f32_16x16x32_f16 v[124:127], v[72:75], v[214:217], v[124:127]
	v_mfma_f32_16x16x32_f16 v[146:149], v[72:75], v[218:221], v[146:149]
	v_mfma_f32_16x16x32_f16 v[134:137], v[72:75], v[226:229], v[134:137]
	v_mfma_f32_16x16x32_f16 v[138:141], v[68:71], v[218:221], v[138:141]
	v_mfma_f32_16x16x32_f16 v[142:145], v[68:71], v[222:225], v[142:145]
	v_mfma_f32_16x16x32_f16 v[150:153], v[72:75], v[222:225], v[150:153]
	s_setprio 0
	ds_read_b128 v[72:75], v129 offset:40960
	ds_read_b128 v[76:79], v129 offset:43008
	v_readfirstlane_b32 s91, v101
	v_lshl_add_u64 v[68:69], v[198:199], 0, s[60:61]
	s_mov_b32 m0, s91
	v_cvt_pk_f16_f32 v15, v14, v15
	global_load_lds_dwordx4 v[68:69], off
	v_cvt_pk_f16_f32 v14, v12, v13
	ds_write_b64 v100, v[14:15] offset:8192
	s_add_u32 s80, s22, 0x40800
	s_addc_u32 s81, s90, 0
	s_add_u32 s100, s22, 0x800
	s_addc_u32 s101, s90, 0
	global_load_dwordx4 v[0:3], v201, s[100:101] nt
	s_setprio 1
	s_waitcnt lgkmcnt(1)
	v_mfma_f32_16x16x32_f16 v[12:15], v[72:75], v[214:217], v[86:89]
	v_mfma_f32_16x16x32_f16 v[170:173], v[72:75], v[218:221], v[170:173]
	v_mfma_f32_16x16x32_f16 v[174:177], v[72:75], v[222:225], v[174:177]
	v_mfma_f32_16x16x32_f16 v[162:165], v[72:75], v[226:229], v[162:165]
	v_mfma_f32_16x16x32_f16 v[178:181], v[76:79], v[214:217], v[178:181]
	v_mfma_f32_16x16x32_f16 v[182:185], v[76:79], v[218:221], v[182:185]
	v_mfma_f32_16x16x32_f16 v[186:189], v[76:79], v[222:225], v[186:189]
	v_mfma_f32_16x16x32_f16 v[154:157], v[76:79], v[226:229], v[154:157]
	s_setprio 0
	ds_read_b128 v[76:79], v129 offset:45056
	ds_read_b128 v[80:83], v129 offset:47104
	v_readfirstlane_b32 s73, v102
	v_lshl_add_u64 v[72:73], v[198:199], 0, s[62:63]
	s_mov_b32 m0, s73
	v_cvt_pk_f16_f32 v19, v18, v19
	global_load_lds_dwordx4 v[72:73], off
	v_cvt_pk_f16_f32 v18, v16, v17
	ds_write_b64 v100, v[18:19] offset:12288
	s_add_u32 s80, s22, 0x60800
	s_addc_u32 s81, s90, 0
	s_add_u32 s100, s22, 0x20800
	s_addc_u32 s101, s90, 0
	global_load_dwordx4 v[64:67], v201, s[100:101] nt
	s_setprio 1
	s_waitcnt lgkmcnt(1)
	v_mfma_f32_16x16x32_f16 v[16:19], v[76:79], v[214:217], v[242:245]
	v_mfma_f32_16x16x32_f16 v[242:245], v[76:79], v[218:221], v[90:93]
	v_mfma_f32_16x16x32_f16 v[158:161], v[76:79], v[222:225], v[158:161]
	v_mfma_f32_16x16x32_f16 v[166:169], v[76:79], v[226:229], v[166:169]
	v_mfma_f32_16x16x32_f16 v[190:193], v[80:83], v[214:217], v[190:193]
	v_mfma_f32_16x16x32_f16 v[202:205], v[80:83], v[218:221], v[202:205]
	v_mfma_f32_16x16x32_f16 v[206:209], v[80:83], v[222:225], v[206:209]
	v_mfma_f32_16x16x32_f16 v[210:213], v[80:83], v[226:229], v[210:213]
	s_setprio 0
	ds_read_b128 v[214:217], v128 offset:32768
	ds_read_b128 v[218:221], v128 offset:34816
	ds_read_b128 v[222:225], v128 offset:36864
	ds_read_b128 v[226:229], v128 offset:38912
	ds_read_b128 v[80:83], v130 offset:32768
	ds_read_b128 v[84:87], v130 offset:34816
	v_cvt_pk_f16_f32 v23, v22, v23
	v_cvt_pk_f16_f32 v22, v20, v21
	ds_write_b64 v100, v[22:23] offset:16384
	s_add_u32 s80, s22, 0x80800
	s_addc_u32 s81, s90, 0
	s_add_u32 s100, s22, 0x40800
	s_addc_u32 s101, s90, 0
	global_load_dwordx4 v[68:71], v201, s[100:101] nt
	s_setprio 1
	s_waitcnt lgkmcnt(1)
	v_mfma_f32_16x16x32_f16 v[20:23], v[80:83], v[214:217], v[246:249]
	v_mfma_f32_16x16x32_f16 v[104:107], v[80:83], v[222:225], v[104:107]
	v_mfma_f32_16x16x32_f16 v[108:111], v[84:87], v[214:217], v[108:111]
	v_mfma_f32_16x16x32_f16 v[112:115], v[84:87], v[218:221], v[112:115]
	v_mfma_f32_16x16x32_f16 v[116:119], v[84:87], v[222:225], v[116:119]
	v_mfma_f32_16x16x32_f16 v[230:233], v[80:83], v[218:221], v[230:233]
	v_mfma_f32_16x16x32_f16 v[234:237], v[80:83], v[226:229], v[234:237]
	v_mfma_f32_16x16x32_f16 v[238:241], v[84:87], v[226:229], v[238:241]
	s_setprio 0
	ds_read_b128 v[84:87], v130 offset:36864
	ds_read_b128 v[88:91], v130 offset:38912
	v_cvt_pk_f16_f32 v27, v26, v27
	v_cvt_pk_f16_f32 v26, v24, v25
	ds_write_b64 v100, v[26:27] offset:20480
	s_add_u32 s80, s22, 0xa0800
	s_addc_u32 s81, s90, 0
	s_add_u32 s100, s22, 0x60800
	s_addc_u32 s101, s90, 0
	global_load_dwordx4 v[72:75], v201, s[100:101] nt
	s_setprio 1
	s_waitcnt lgkmcnt(1)
	v_mfma_f32_16x16x32_f16 v[24:27], v[84:87], v[214:217], v[8:11]
	v_mfma_f32_16x16x32_f16 v[120:123], v[84:87], v[226:229], v[120:123]
	v_mfma_f32_16x16x32_f16 v[124:127], v[88:91], v[214:217], v[124:127]
	v_mfma_f32_16x16x32_f16 v[146:149], v[88:91], v[218:221], v[146:149]
	v_mfma_f32_16x16x32_f16 v[134:137], v[88:91], v[226:229], v[134:137]
	v_mfma_f32_16x16x32_f16 v[138:141], v[84:87], v[218:221], v[138:141]
	v_mfma_f32_16x16x32_f16 v[142:145], v[84:87], v[222:225], v[142:145]
	v_mfma_f32_16x16x32_f16 v[150:153], v[88:91], v[222:225], v[150:153]
	s_setprio 0
	ds_read_b128 v[8:11], v130 offset:40960
	ds_read_b128 v[88:91], v130 offset:43008
	v_cvt_pk_f16_f32 v31, v30, v31
	v_cvt_pk_f16_f32 v30, v28, v29
	ds_write_b64 v100, v[30:31] offset:24576
	s_add_u32 s80, s22, 0xc0800
	s_addc_u32 s81, s90, 0
	s_add_u32 s100, s22, 0x80800
	s_addc_u32 s101, s90, 0
	global_load_dwordx4 v[76:79], v201, s[100:101] nt
	s_add_u32 s100, s22, 0xa0800
	s_addc_u32 s101, s90, 0
	global_load_dwordx4 v[80:83], v201, s[100:101] nt
	s_setprio 1
	s_waitcnt lgkmcnt(1)
	v_mfma_f32_16x16x32_f16 v[12:15], v[8:11], v[214:217], v[12:15]
	v_mfma_f32_16x16x32_f16 v[28:31], v[8:11], v[218:221], v[170:173]
	v_mfma_f32_16x16x32_f16 v[170:173], v[8:11], v[222:225], v[174:177]
	v_mfma_f32_16x16x32_f16 v[162:165], v[8:11], v[226:229], v[162:165]
	v_mfma_f32_16x16x32_f16 v[174:177], v[88:91], v[214:217], v[178:181]
	v_mfma_f32_16x16x32_f16 v[178:181], v[88:91], v[218:221], v[182:185]
	v_mfma_f32_16x16x32_f16 v[182:185], v[88:91], v[222:225], v[186:189]
	v_mfma_f32_16x16x32_f16 v[154:157], v[88:91], v[226:229], v[154:157]
	s_setprio 0
	ds_read_b128 v[8:11], v130 offset:45056
	ds_read_b128 v[186:189], v130 offset:47104
	v_cvt_pk_f16_f32 v35, v34, v35
	v_cvt_pk_f16_f32 v34, v32, v33
	ds_write_b64 v100, v[34:35] offset:28672
	s_add_u32 s80, s22, 0xe0800
	s_addc_u32 s81, s90, 0
	s_add_u32 s100, s22, 0xc0800
	s_addc_u32 s101, s90, 0
	global_load_dwordx4 v[84:87], v201, s[100:101] nt
	s_add_u32 s100, s22, 0xe0800
	s_addc_u32 s101, s90, 0
	global_load_dwordx4 v[88:91], v201, s[100:101] nt
	s_setprio 1
	s_waitcnt lgkmcnt(1)
	v_mfma_f32_16x16x32_f16 v[16:19], v[8:11], v[214:217], v[16:19]
	v_mfma_f32_16x16x32_f16 v[32:35], v[8:11], v[218:221], v[242:245]
	v_mfma_f32_16x16x32_f16 v[158:161], v[8:11], v[222:225], v[158:161]
	v_mfma_f32_16x16x32_f16 v[166:169], v[8:11], v[226:229], v[166:169]
	v_mfma_f32_16x16x32_f16 v[190:193], v[186:189], v[214:217], v[190:193]
	v_mfma_f32_16x16x32_f16 v[202:205], v[186:189], v[218:221], v[202:205]
	v_mfma_f32_16x16x32_f16 v[206:209], v[186:189], v[222:225], v[206:209]
	v_mfma_f32_16x16x32_f16 v[186:189], v[186:189], v[226:229], v[210:213]
	s_setprio 0
	s_waitcnt vmcnt(7)
	s_waitcnt lgkmcnt(0)
	s_barrier
	s_nop 0
	ds_read_b128 v[210:213], v131
	ds_read_b128 v[214:217], v131 offset:2048
	ds_read_b128 v[218:221], v131 offset:4096
	ds_read_b128 v[222:225], v131 offset:6144
	ds_read_b128 v[8:11], v129
	ds_read_b128 v[226:229], v129 offset:2048
	s_add_u32 s80, s22, 0x900
	v_lshl_add_u64 v[92:93], s[40:41], 0, v[196:197]
	s_addc_u32 s81, s90, 0
	v_cvt_pk_f16_f32 v7, v6, v7
	s_cmp_lg_u32 s2, 0
	s_cbranch_scc1 .Lres_skip_0
	s_add_u32 m0, s0, 0x18000
	s_nop 0
	global_load_lds_dwordx4 v[92:93], off

.Lres_skip_1:
	v_cvt_pk_f16_f32 v9, v42, v43
	v_cvt_pk_f16_f32 v8, v40, v41
	ds_write_b64 v100, v[8:9] offset:36864
	s_add_u32 s80, s22, 0x20900
	s_addc_u32 s81, s90, 0
	s_setprio 1
	s_waitcnt lgkmcnt(1)
	v_mfma_f32_16x16x32_f16 v[24:27], v[238:241], v[210:213], v[24:27]
	v_mfma_f32_16x16x32_f16 v[120:123], v[238:241], v[222:225], v[120:123]
	v_mfma_f32_16x16x32_f16 v[124:127], v[242:245], v[210:213], v[124:127]
	v_mfma_f32_16x16x32_f16 v[146:149], v[242:245], v[214:217], v[146:149]
	v_mfma_f32_16x16x32_f16 v[134:137], v[242:245], v[222:225], v[134:137]
	v_mfma_f32_16x16x32_f16 v[138:141], v[238:241], v[214:217], v[138:141]
	v_mfma_f32_16x16x32_f16 v[142:145], v[238:241], v[218:221], v[142:145]
	v_mfma_f32_16x16x32_f16 v[150:153], v[242:245], v[218:221], v[150:153]
	s_setprio 0
	ds_read_b128 v[238:241], v129 offset:8192
	ds_read_b128 v[242:245], v129 offset:10240
	s_cmp_lg_u32 s2, 0
	s_cbranch_scc1 .Lres_skip_2
	s_add_u32 m0, s71, 0x18000
	s_nop 0
	v_lshl_add_u64 v[40:41], v[92:93], 0, s[60:61]
	global_load_lds_dwordx4 v[40:41], off
.Lres_skip_2:
	v_cvt_pk_f16_f32 v41, v46, v47
	v_cvt_pk_f16_f32 v40, v44, v45
	ds_write_b64 v100, v[40:41] offset:40960
	s_add_u32 s80, s22, 0x40900
	s_addc_u32 s81, s90, 0
	s_add_u32 s100, s22, 0x900
	s_addc_u32 s101, s90, 0
	global_load_dwordx4 v[4:7], v201, s[100:101] nt
	s_setprio 1
	s_waitcnt lgkmcnt(1)
	v_mfma_f32_16x16x32_f16 v[12:15], v[238:241], v[210:213], v[12:15]
	v_mfma_f32_16x16x32_f16 v[28:31], v[238:241], v[214:217], v[28:31]
	v_mfma_f32_16x16x32_f16 v[170:173], v[238:241], v[218:221], v[170:173]
	v_mfma_f32_16x16x32_f16 v[162:165], v[238:241], v[222:225], v[162:165]
	v_mfma_f32_16x16x32_f16 v[174:177], v[242:245], v[210:213], v[174:177]
	v_mfma_f32_16x16x32_f16 v[178:181], v[242:245], v[214:217], v[178:181]
	v_mfma_f32_16x16x32_f16 v[182:185], v[242:245], v[218:221], v[182:185]
	v_mfma_f32_16x16x32_f16 v[154:157], v[242:245], v[222:225], v[154:157]
	s_setprio 0
	ds_read_b128 v[238:241], v129 offset:12288
	ds_read_b128 v[242:245], v129 offset:14336
	s_cmp_lg_u32 s2, 0
	s_cbranch_scc1 .Lres_skip_3
	s_add_u32 m0, s70, 0x18000
	s_nop 0
	v_lshl_add_u64 v[44:45], v[92:93], 0, s[62:63]
	global_load_lds_dwordx4 v[44:45], off
.Lres_skip_3:
	v_cvt_pk_f16_f32 v45, v50, v51
	v_cvt_pk_f16_f32 v44, v48, v49
	ds_write_b64 v100, v[44:45] offset:45056
	s_add_u32 s70, s22, 0x60900
	s_addc_u32 s71, s90, 0
	s_add_u32 s100, s22, 0x20900
	s_addc_u32 s101, s90, 0
	global_load_dwordx4 v[8:11], v201, s[100:101] nt
	s_setprio 1
	s_waitcnt lgkmcnt(1)
	v_mfma_f32_16x16x32_f16 v[16:19], v[238:241], v[210:213], v[16:19]
	v_mfma_f32_16x16x32_f16 v[32:35], v[238:241], v[214:217], v[32:35]
	v_mfma_f32_16x16x32_f16 v[158:161], v[238:241], v[218:221], v[158:161]
	v_mfma_f32_16x16x32_f16 v[166:169], v[238:241], v[222:225], v[166:169]
	v_mfma_f32_16x16x32_f16 v[190:193], v[242:245], v[210:213], v[190:193]
	v_mfma_f32_16x16x32_f16 v[202:205], v[242:245], v[214:217], v[202:205]
	v_mfma_f32_16x16x32_f16 v[206:209], v[242:245], v[218:221], v[206:209]
	v_mfma_f32_16x16x32_f16 v[186:189], v[242:245], v[222:225], v[186:189]
	s_setprio 0
	ds_read_b128 v[210:213], v128
	ds_read_b128 v[214:217], v128 offset:2048
	ds_read_b128 v[218:221], v128 offset:4096
	ds_read_b128 v[222:225], v128 offset:6144
	ds_read_b128 v[238:241], v130
	ds_read_b128 v[242:245], v130 offset:2048
	v_cvt_pk_f16_f32 v49, v54, v55
	v_cvt_pk_f16_f32 v48, v52, v53
	ds_write_b64 v100, v[48:49] offset:49152
	s_add_u32 s70, s22, 0x80900
	s_addc_u32 s71, s90, 0
	s_add_u32 s100, s22, 0x40900
	s_addc_u32 s101, s90, 0
	global_load_dwordx4 v[40:43], v201, s[100:101] nt
	s_setprio 1
	s_waitcnt lgkmcnt(1)
	v_mfma_f32_16x16x32_f16 v[20:23], v[238:241], v[210:213], v[20:23]
	v_mfma_f32_16x16x32_f16 v[104:107], v[238:241], v[218:221], v[104:107]
	v_mfma_f32_16x16x32_f16 v[108:111], v[242:245], v[210:213], v[108:111]
	v_mfma_f32_16x16x32_f16 v[112:115], v[242:245], v[214:217], v[112:115]
	v_mfma_f32_16x16x32_f16 v[116:119], v[242:245], v[218:221], v[116:119]
	v_mfma_f32_16x16x32_f16 v[230:233], v[238:241], v[214:217], v[230:233]
	v_mfma_f32_16x16x32_f16 v[234:237], v[238:241], v[222:225], v[234:237]
	v_mfma_f32_16x16x32_f16 v[226:229], v[242:245], v[222:225], v[226:229]
	s_setprio 0
	ds_read_b128 v[238:241], v130 offset:4096
	ds_read_b128 v[242:245], v130 offset:6144
	v_cvt_pk_f16_f32 v53, v58, v59
	v_cvt_pk_f16_f32 v52, v56, v57
	ds_write_b64 v100, v[52:53] offset:53248
	s_add_u32 s70, s22, 0xa0900
	s_addc_u32 s71, s90, 0
	s_add_u32 s100, s22, 0x60900
	s_addc_u32 s101, s90, 0
	global_load_dwordx4 v[44:47], v201, s[100:101] nt
	s_setprio 1
	s_waitcnt lgkmcnt(1)
	v_mfma_f32_16x16x32_f16 v[24:27], v[238:241], v[210:213], v[24:27]
	v_mfma_f32_16x16x32_f16 v[120:123], v[238:241], v[222:225], v[120:123]
	v_mfma_f32_16x16x32_f16 v[124:127], v[242:245], v[210:213], v[124:127]
	v_mfma_f32_16x16x32_f16 v[146:149], v[242:245], v[214:217], v[146:149]
	v_mfma_f32_16x16x32_f16 v[134:137], v[242:245], v[222:225], v[134:137]
	v_mfma_f32_16x16x32_f16 v[138:141], v[238:241], v[214:217], v[138:141]
	v_mfma_f32_16x16x32_f16 v[142:145], v[238:241], v[218:221], v[142:145]
	v_mfma_f32_16x16x32_f16 v[150:153], v[242:245], v[218:221], v[150:153]
	s_setprio 0
	ds_read_b128 v[238:241], v130 offset:8192
	ds_read_b128 v[242:245], v130 offset:10240
	v_cvt_pk_f16_f32 v57, v62, v63
	v_cvt_pk_f16_f32 v56, v60, v61
	ds_write_b64 v100, v[56:57] offset:57344
	s_add_u32 s70, s22, 0xc0900
	s_addc_u32 s71, s90, 0
	s_add_u32 s100, s22, 0x80900
	s_addc_u32 s101, s90, 0
	global_load_dwordx4 v[48:51], v201, s[100:101] nt
	s_add_u32 s100, s22, 0xa0900
	s_addc_u32 s101, s90, 0
	global_load_dwordx4 v[52:55], v201, s[100:101] nt
	s_setprio 1
	s_waitcnt lgkmcnt(1)
	v_mfma_f32_16x16x32_f16 v[28:31], v[238:241], v[214:217], v[28:31]
	v_mfma_f32_16x16x32_f16 v[246:249], v[238:241], v[210:213], v[12:15]
	v_mfma_f32_16x16x32_f16 v[170:173], v[238:241], v[218:221], v[170:173]
	v_mfma_f32_16x16x32_f16 v[162:165], v[238:241], v[222:225], v[162:165]
	v_mfma_f32_16x16x32_f16 v[174:177], v[242:245], v[210:213], v[174:177]
	v_mfma_f32_16x16x32_f16 v[178:181], v[242:245], v[214:217], v[178:181]
	v_mfma_f32_16x16x32_f16 v[182:185], v[242:245], v[218:221], v[182:185]
	v_mfma_f32_16x16x32_f16 v[154:157], v[242:245], v[222:225], v[154:157]
	s_setprio 0
	ds_read_b128 v[12:15], v130 offset:12288
	ds_read_b128 v[238:241], v130 offset:14336
	v_cvt_pk_f16_f32 v39, v38, v39
	v_cvt_pk_f16_f32 v38, v36, v37
	ds_write_b64 v100, v[38:39] offset:61440
	s_add_u32 s70, s22, 0xe0900
	s_addc_u32 s71, s90, 0
	s_add_u32 s100, s22, 0xc0900
	s_addc_u32 s101, s90, 0
	global_load_dwordx4 v[56:59], v201, s[100:101] nt
	s_add_u32 s100, s22, 0xe0900
	s_addc_u32 s101, s90, 0
	global_load_dwordx4 v[60:63], v201, s[100:101] nt
	s_setprio 1
	s_waitcnt lgkmcnt(1)
	v_mfma_f32_16x16x32_f16 v[36:39], v[12:15], v[210:213], v[16:19]
	v_mfma_f32_16x16x32_f16 v[32:35], v[12:15], v[214:217], v[32:35]
	v_mfma_f32_16x16x32_f16 v[158:161], v[12:15], v[218:221], v[158:161]
	v_mfma_f32_16x16x32_f16 v[166:169], v[12:15], v[222:225], v[166:169]
	v_mfma_f32_16x16x32_f16 v[190:193], v[238:241], v[210:213], v[190:193]
	v_mfma_f32_16x16x32_f16 v[202:205], v[238:241], v[214:217], v[202:205]
	v_mfma_f32_16x16x32_f16 v[206:209], v[238:241], v[218:221], v[206:209]
	v_mfma_f32_16x16x32_f16 v[186:189], v[238:241], v[222:225], v[186:189]
	s_setprio 0
	s_waitcnt vmcnt(7)
	s_waitcnt lgkmcnt(0)
	s_barrier
	v_add_u32_e32 v250, 0x20000, v129
	v_add_u32_e32 v251, 0x20000, v130
	ds_read_b128 v[210:213], v131 offset:32768
	ds_read_b128 v[214:217], v131 offset:34816
	ds_read_b128 v[218:221], v131 offset:36864
	ds_read_b128 v[222:225], v131 offset:38912
	ds_read_b128 v[12:15], v250
	ds_read_b128 v[16:19], v250 offset:2048
	s_add_u32 s70, s22, 0xa00
	v_lshl_add_u64 v[92:93], s[42:43], 0, v[196:197]
	s_addc_u32 s71, s90, 0
	s_mov_b32 m0, s1
	v_cvt_pk_f16_f32 v3, v2, v3
	global_load_lds_dwordx4 v[92:93], off
	v_cvt_pk_f16_f32 v2, v0, v1
	ds_write_b64 v100, v[2:3]
	s_setprio 1
	s_waitcnt lgkmcnt(1)
	v_mfma_f32_16x16x32_f16 v[104:107], v[12:15], v[218:221], v[104:107]
	v_mfma_f32_16x16x32_f16 v[108:111], v[16:19], v[210:213], v[108:111]
	v_mfma_f32_16x16x32_f16 v[112:115], v[16:19], v[214:217], v[112:115]
	v_mfma_f32_16x16x32_f16 v[116:119], v[16:19], v[218:221], v[116:119]
	v_mfma_f32_16x16x32_f16 v[238:241], v[12:15], v[210:213], v[20:23]
	v_mfma_f32_16x16x32_f16 v[230:233], v[12:15], v[214:217], v[230:233]
	v_mfma_f32_16x16x32_f16 v[234:237], v[12:15], v[222:225], v[234:237]
	v_mfma_f32_16x16x32_f16 v[226:229], v[16:19], v[222:225], v[226:229]
	s_setprio 0
	ds_read_b128 v[16:19], v250 offset:4096
	ds_read_b128 v[20:23], v250 offset:6144
	s_mov_b32 m0, s92
	v_lshl_add_u64 v[12:13], v[92:93], 0, s[58:59]
	global_load_lds_dwordx4 v[12:13], off
	v_cvt_pk_f16_f32 v13, v66, v67
	v_cvt_pk_f16_f32 v12, v64, v65
	ds_write_b64 v100, v[12:13] offset:4096
	s_add_u32 s0, s22, 0x20a00
	s_addc_u32 s1, s90, 0
	s_setprio 1
	s_waitcnt lgkmcnt(1)
	v_mfma_f32_16x16x32_f16 v[64:67], v[16:19], v[210:213], v[24:27]
	v_mfma_f32_16x16x32_f16 v[120:123], v[16:19], v[222:225], v[120:123]
	v_mfma_f32_16x16x32_f16 v[124:127], v[20:23], v[210:213], v[124:127]
	v_mfma_f32_16x16x32_f16 v[146:149], v[20:23], v[214:217], v[146:149]
	v_mfma_f32_16x16x32_f16 v[134:137], v[20:23], v[222:225], v[134:137]
	v_mfma_f32_16x16x32_f16 v[138:141], v[16:19], v[214:217], v[138:141]
	v_mfma_f32_16x16x32_f16 v[142:145], v[16:19], v[218:221], v[142:145]
	v_mfma_f32_16x16x32_f16 v[150:153], v[20:23], v[218:221], v[150:153]
	s_setprio 0
	ds_read_b128 v[20:23], v250 offset:8192
	ds_read_b128 v[24:27], v250 offset:10240
	s_mov_b32 m0, s91
	v_lshl_add_u64 v[16:17], v[92:93], 0, s[60:61]
	global_load_lds_dwordx4 v[16:17], off
	v_cvt_pk_f16_f32 v17, v70, v71
	v_cvt_pk_f16_f32 v16, v68, v69
	ds_write_b64 v100, v[16:17] offset:8192
	s_add_u32 s0, s22, 0x40a00
	s_addc_u32 s1, s90, 0
	s_add_u32 s100, s22, 0xa00
	s_addc_u32 s101, s90, 0
	global_load_dwordx4 v[0:3], v201, s[100:101] nt
	s_setprio 1
	s_waitcnt lgkmcnt(1)
	v_mfma_f32_16x16x32_f16 v[68:71], v[20:23], v[210:213], v[246:249]
	v_mfma_f32_16x16x32_f16 v[242:245], v[20:23], v[214:217], v[28:31]
	v_mfma_f32_16x16x32_f16 v[170:173], v[20:23], v[218:221], v[170:173]
	v_mfma_f32_16x16x32_f16 v[162:165], v[20:23], v[222:225], v[162:165]
	v_mfma_f32_16x16x32_f16 v[174:177], v[24:27], v[210:213], v[174:177]
	v_mfma_f32_16x16x32_f16 v[178:181], v[24:27], v[214:217], v[178:181]
	v_mfma_f32_16x16x32_f16 v[182:185], v[24:27], v[218:221], v[182:185]
	v_mfma_f32_16x16x32_f16 v[154:157], v[24:27], v[222:225], v[154:157]
	s_setprio 0
	ds_read_b128 v[24:27], v250 offset:12288
	ds_read_b128 v[28:31], v250 offset:14336
	s_mov_b32 m0, s73
	v_lshl_add_u64 v[20:21], v[92:93], 0, s[62:63]
	global_load_lds_dwordx4 v[20:21], off
	v_cvt_pk_f16_f32 v21, v74, v75
	v_cvt_pk_f16_f32 v20, v72, v73
	ds_write_b64 v100, v[20:21] offset:12288
	s_add_u32 s0, s22, 0x60a00
	s_addc_u32 s1, s90, 0
	s_add_u32 s100, s22, 0x20a00
	s_addc_u32 s101, s90, 0
	global_load_dwordx4 v[12:15], v201, s[100:101] nt
	s_setprio 1
	s_waitcnt lgkmcnt(1)
	v_mfma_f32_16x16x32_f16 v[72:75], v[24:27], v[210:213], v[36:39]
	v_mfma_f32_16x16x32_f16 v[246:249], v[24:27], v[214:217], v[32:35]
	v_mfma_f32_16x16x32_f16 v[158:161], v[24:27], v[218:221], v[158:161]
	v_mfma_f32_16x16x32_f16 v[166:169], v[24:27], v[222:225], v[166:169]
	v_mfma_f32_16x16x32_f16 v[190:193], v[28:31], v[210:213], v[190:193]
	v_mfma_f32_16x16x32_f16 v[202:205], v[28:31], v[214:217], v[202:205]
	v_mfma_f32_16x16x32_f16 v[206:209], v[28:31], v[218:221], v[206:209]
	v_mfma_f32_16x16x32_f16 v[186:189], v[28:31], v[222:225], v[186:189]
	s_setprio 0
	ds_read_b128 v[210:213], v128 offset:32768
	ds_read_b128 v[214:217], v128 offset:34816
	ds_read_b128 v[218:221], v128 offset:36864
	ds_read_b128 v[222:225], v128 offset:38912
	ds_read_b128 v[28:31], v251
	ds_read_b128 v[32:35], v251 offset:2048
	v_cvt_pk_f16_f32 v25, v78, v79
	v_cvt_pk_f16_f32 v24, v76, v77
	ds_write_b64 v100, v[24:25] offset:16384
	s_add_u32 s0, s22, 0x80a00
	s_addc_u32 s1, s90, 0
	s_add_u32 s100, s22, 0x40a00
	s_addc_u32 s101, s90, 0
	global_load_dwordx4 v[16:19], v201, s[100:101] nt
	s_setprio 1
	s_waitcnt lgkmcnt(1)
	v_mfma_f32_16x16x32_f16 v[76:79], v[28:31], v[210:213], v[238:241]
	v_mfma_f32_16x16x32_f16 v[104:107], v[28:31], v[218:221], v[104:107]
	v_mfma_f32_16x16x32_f16 v[108:111], v[32:35], v[210:213], v[108:111]
	v_mfma_f32_16x16x32_f16 v[112:115], v[32:35], v[214:217], v[112:115]
	v_mfma_f32_16x16x32_f16 v[116:119], v[32:35], v[218:221], v[116:119]
	v_mfma_f32_16x16x32_f16 v[230:233], v[28:31], v[214:217], v[230:233]
	v_mfma_f32_16x16x32_f16 v[234:237], v[28:31], v[222:225], v[234:237]
	v_mfma_f32_16x16x32_f16 v[226:229], v[32:35], v[222:225], v[226:229]
	s_setprio 0
	ds_read_b128 v[32:35], v251 offset:4096
	ds_read_b128 v[36:39], v251 offset:6144
	v_cvt_pk_f16_f32 v29, v82, v83
	v_cvt_pk_f16_f32 v28, v80, v81
	ds_write_b64 v100, v[28:29] offset:20480
	s_add_u32 s0, s22, 0xa0a00
	s_addc_u32 s1, s90, 0
	s_add_u32 s100, s22, 0x60a00
	s_addc_u32 s101, s90, 0
	global_load_dwordx4 v[20:23], v201, s[100:101] nt
	s_setprio 1
	s_waitcnt lgkmcnt(1)
	v_mfma_f32_16x16x32_f16 v[80:83], v[32:35], v[210:213], v[64:67]
	v_mfma_f32_16x16x32_f16 v[120:123], v[32:35], v[222:225], v[120:123]
	v_mfma_f32_16x16x32_f16 v[124:127], v[36:39], v[210:213], v[124:127]
	v_mfma_f32_16x16x32_f16 v[146:149], v[36:39], v[214:217], v[146:149]
	v_mfma_f32_16x16x32_f16 v[134:137], v[36:39], v[222:225], v[134:137]
	v_mfma_f32_16x16x32_f16 v[138:141], v[32:35], v[214:217], v[138:141]
	v_mfma_f32_16x16x32_f16 v[142:145], v[32:35], v[218:221], v[142:145]
	v_mfma_f32_16x16x32_f16 v[150:153], v[36:39], v[218:221], v[150:153]
	s_setprio 0
	ds_read_b128 v[36:39], v251 offset:8192
	ds_read_b128 v[64:67], v251 offset:10240
	v_cvt_pk_f16_f32 v33, v86, v87
	v_cvt_pk_f16_f32 v32, v84, v85
	ds_write_b64 v100, v[32:33] offset:24576
	s_add_u32 s0, s22, 0xc0a00
	s_addc_u32 s1, s90, 0
	s_add_u32 s100, s22, 0x80a00
	s_addc_u32 s101, s90, 0
	global_load_dwordx4 v[24:27], v201, s[100:101] nt
	s_add_u32 s100, s22, 0xa0a00
	s_addc_u32 s101, s90, 0
	global_load_dwordx4 v[28:31], v201, s[100:101] nt
	s_setprio 1
	s_waitcnt lgkmcnt(1)
	v_mfma_f32_16x16x32_f16 v[68:71], v[36:39], v[210:213], v[68:71]
	v_mfma_f32_16x16x32_f16 v[84:87], v[36:39], v[214:217], v[242:245]
	v_mfma_f32_16x16x32_f16 v[170:173], v[36:39], v[218:221], v[170:173]
	v_mfma_f32_16x16x32_f16 v[162:165], v[36:39], v[222:225], v[162:165]
	v_mfma_f32_16x16x32_f16 v[174:177], v[64:67], v[210:213], v[174:177]
	v_mfma_f32_16x16x32_f16 v[178:181], v[64:67], v[214:217], v[178:181]
	v_mfma_f32_16x16x32_f16 v[182:185], v[64:67], v[218:221], v[182:185]
	v_mfma_f32_16x16x32_f16 v[154:157], v[64:67], v[222:225], v[154:157]
	s_setprio 0
	ds_read_b128 v[64:67], v251 offset:12288
	ds_read_b128 v[238:241], v251 offset:14336
	v_cvt_pk_f16_f32 v37, v90, v91
	v_cvt_pk_f16_f32 v36, v88, v89
	ds_write_b64 v100, v[36:37] offset:28672
	s_add_u32 s0, s22, 0xe0a00
	s_addc_u32 s1, s90, 0
	s_add_u32 s100, s22, 0xc0a00
	s_addc_u32 s101, s90, 0
	global_load_dwordx4 v[32:35], v201, s[100:101] nt
	s_add_u32 s100, s22, 0xe0a00
	s_addc_u32 s101, s90, 0
	global_load_dwordx4 v[36:39], v201, s[100:101] nt
	s_setprio 1
	s_waitcnt lgkmcnt(1)
	v_mfma_f32_16x16x32_f16 v[72:75], v[64:67], v[210:213], v[72:75]
	v_mfma_f32_16x16x32_f16 v[88:91], v[64:67], v[214:217], v[246:249]
	v_mfma_f32_16x16x32_f16 v[158:161], v[64:67], v[218:221], v[158:161]
	v_mfma_f32_16x16x32_f16 v[166:169], v[64:67], v[222:225], v[166:169]
	v_mfma_f32_16x16x32_f16 v[190:193], v[238:241], v[210:213], v[190:193]
	v_mfma_f32_16x16x32_f16 v[202:205], v[238:241], v[214:217], v[202:205]
	v_mfma_f32_16x16x32_f16 v[206:209], v[238:241], v[218:221], v[206:209]
	v_mfma_f32_16x16x32_f16 v[186:189], v[238:241], v[222:225], v[186:189]
	s_setprio 0
	s_waitcnt vmcnt(7)
	s_waitcnt lgkmcnt(0)
	s_barrier
	ds_read_b128 v[210:213], v131
	ds_read_b128 v[214:217], v131 offset:2048
	ds_read_b128 v[218:221], v131 offset:4096
	ds_read_b128 v[222:225], v131 offset:6144
	ds_read_b128 v[64:67], v129
	ds_read_b128 v[238:241], v129 offset:2048
	s_add_u32 s70, s22, 0xb00
	v_lshl_add_u64 v[92:93], s[44:45], 0, v[196:197]
	s_addc_u32 s71, s90, 0
	v_readfirstlane_b32 s0, v95
	s_mov_b32 m0, s0
	v_cvt_pk_f16_f32 v7, v6, v7
	global_load_lds_dwordx4 v[92:93], off
	v_cvt_pk_f16_f32 v6, v4, v5
	ds_write_b64 v100, v[6:7] offset:32768
	s_setprio 1
	s_waitcnt lgkmcnt(1)
	v_mfma_f32_16x16x32_f16 v[76:79], v[64:67], v[210:213], v[76:79]
	v_mfma_f32_16x16x32_f16 v[104:107], v[64:67], v[218:221], v[104:107]
	v_mfma_f32_16x16x32_f16 v[108:111], v[238:241], v[210:213], v[108:111]
	v_mfma_f32_16x16x32_f16 v[112:115], v[238:241], v[214:217], v[112:115]
	v_mfma_f32_16x16x32_f16 v[116:119], v[238:241], v[218:221], v[116:119]
	v_mfma_f32_16x16x32_f16 v[230:233], v[64:67], v[214:217], v[230:233]
	v_mfma_f32_16x16x32_f16 v[234:237], v[64:67], v[222:225], v[234:237]
	v_mfma_f32_16x16x32_f16 v[226:229], v[238:241], v[222:225], v[226:229]
	s_setprio 0
	ds_read_b128 v[238:241], v129 offset:4096
	ds_read_b128 v[242:245], v129 offset:6144
	v_readfirstlane_b32 s72, v96
	v_lshl_add_u64 v[64:65], v[92:93], 0, s[58:59]
	s_mov_b32 m0, s72
	v_cvt_pk_f16_f32 v11, v10, v11
	global_load_lds_dwordx4 v[64:65], off
	v_cvt_pk_f16_f32 v10, v8, v9
	ds_write_b64 v100, v[10:11] offset:36864
	s_add_u32 s70, s22, 0x20b00
	s_addc_u32 s71, s90, 0
	s_setprio 1
	s_waitcnt lgkmcnt(1)
	v_mfma_f32_16x16x32_f16 v[8:11], v[238:241], v[210:213], v[80:83]
	v_mfma_f32_16x16x32_f16 v[80:83], v[238:241], v[214:217], v[138:141]
	v_mfma_f32_16x16x32_f16 v[138:141], v[238:241], v[218:221], v[142:145]
	v_mfma_f32_16x16x32_f16 v[120:123], v[238:241], v[222:225], v[120:123]
	v_mfma_f32_16x16x32_f16 v[124:127], v[242:245], v[210:213], v[124:127]
	v_mfma_f32_16x16x32_f16 v[142:145], v[242:245], v[214:217], v[146:149]
	v_mfma_f32_16x16x32_f16 v[146:149], v[242:245], v[218:221], v[150:153]
	v_mfma_f32_16x16x32_f16 v[134:137], v[242:245], v[222:225], v[134:137]
	s_setprio 0
	s_nop 0
	ds_read_b128 v[150:153], v129 offset:8192
	ds_read_b128 v[238:241], v129 offset:10240
	v_readfirstlane_b32 s71, v97
	v_lshl_add_u64 v[198:199], v[92:93], 0, s[60:61]
	s_mov_b32 m0, s71
	v_cvt_pk_f16_f32 v43, v42, v43
	global_load_lds_dwordx4 v[198:199], off
	v_cvt_pk_f16_f32 v42, v40, v41
	ds_write_b64 v100, v[42:43] offset:40960
	s_add_u32 s80, s22, 0x40b00
	s_addc_u32 s81, s90, 0
	s_add_u32 s100, s22, 0xb00
	s_addc_u32 s101, s90, 0
	global_load_dwordx4 v[4:7], v201, s[100:101] nt
	s_setprio 1
	s_waitcnt lgkmcnt(1)
	v_mfma_f32_16x16x32_f16 v[68:71], v[150:153], v[210:213], v[68:71]
	v_mfma_f32_16x16x32_f16 v[84:87], v[150:153], v[214:217], v[84:87]
	v_mfma_f32_16x16x32_f16 v[170:173], v[150:153], v[218:221], v[170:173]
	v_mfma_f32_16x16x32_f16 v[150:153], v[150:153], v[222:225], v[162:165]
	v_mfma_f32_16x16x32_f16 v[162:165], v[238:241], v[210:213], v[174:177]
	v_mfma_f32_16x16x32_f16 v[174:177], v[238:241], v[214:217], v[178:181]
	v_mfma_f32_16x16x32_f16 v[178:181], v[238:241], v[218:221], v[182:185]
	v_mfma_f32_16x16x32_f16 v[154:157], v[238:241], v[222:225], v[154:157]
	s_setprio 0
	s_nop 0
	ds_read_b128 v[182:185], v129 offset:12288
	ds_read_b128 v[238:241], v129 offset:14336
	v_readfirstlane_b32 s70, v98
	v_lshl_add_u64 v[92:93], v[92:93], 0, s[62:63]
	s_mov_b32 m0, s70
	v_cvt_pk_f16_f32 v47, v46, v47
	global_load_lds_dwordx4 v[92:93], off
	v_cvt_pk_f16_f32 v46, v44, v45
	ds_write_b64 v100, v[46:47] offset:45056
	s_add_u32 s80, s22, 0x60b00
	s_addc_u32 s81, s90, 0
	s_add_u32 s100, s22, 0x20b00
	s_addc_u32 s101, s90, 0
	global_load_dwordx4 v[64:67], v201, s[100:101] nt
	s_setprio 1
	s_waitcnt lgkmcnt(1)
	v_mfma_f32_16x16x32_f16 v[72:75], v[182:185], v[210:213], v[72:75]
	v_mfma_f32_16x16x32_f16 v[88:91], v[182:185], v[214:217], v[88:91]
	v_mfma_f32_16x16x32_f16 v[158:161], v[182:185], v[218:221], v[158:161]
	v_mfma_f32_16x16x32_f16 v[166:169], v[182:185], v[222:225], v[166:169]
	v_mfma_f32_16x16x32_f16 v[182:185], v[238:241], v[210:213], v[190:193]
	v_mfma_f32_16x16x32_f16 v[190:193], v[238:241], v[214:217], v[202:205]
	v_mfma_f32_16x16x32_f16 v[202:205], v[238:241], v[218:221], v[206:209]
	v_mfma_f32_16x16x32_f16 v[186:189], v[238:241], v[222:225], v[186:189]
	s_setprio 0
	s_nop 0
	ds_read_b128 v[206:209], v128
	ds_read_b128 v[210:213], v128 offset:2048
	ds_read_b128 v[214:217], v128 offset:4096
	ds_read_b128 v[218:221], v128 offset:6144
	ds_read_b128 v[222:225], v130
	ds_read_b128 v[238:241], v130 offset:2048
	v_cvt_pk_f16_f32 v51, v50, v51
	v_cvt_pk_f16_f32 v50, v48, v49
	ds_write_b64 v100, v[50:51] offset:49152
	s_add_u32 s80, s22, 0x80b00
	s_addc_u32 s81, s90, 0
	s_add_u32 s100, s22, 0x40b00
	s_addc_u32 s101, s90, 0
	global_load_dwordx4 v[40:43], v201, s[100:101] nt
	s_setprio 1
	s_waitcnt lgkmcnt(1)
	v_mfma_f32_16x16x32_f16 v[76:79], v[222:225], v[206:209], v[76:79]
	v_mfma_f32_16x16x32_f16 v[104:107], v[222:225], v[214:217], v[104:107]
	v_mfma_f32_16x16x32_f16 v[108:111], v[238:241], v[206:209], v[108:111]
	v_mfma_f32_16x16x32_f16 v[112:115], v[238:241], v[210:213], v[112:115]
	v_mfma_f32_16x16x32_f16 v[116:119], v[238:241], v[214:217], v[116:119]
	v_mfma_f32_16x16x32_f16 v[230:233], v[222:225], v[210:213], v[230:233]
	v_mfma_f32_16x16x32_f16 v[222:225], v[222:225], v[218:221], v[234:237]
	v_mfma_f32_16x16x32_f16 v[226:229], v[238:241], v[218:221], v[226:229]
	s_setprio 0
	s_nop 0
	ds_read_b128 v[234:237], v130 offset:4096
	ds_read_b128 v[238:241], v130 offset:6144
	v_cvt_pk_f16_f32 v55, v54, v55
	v_cvt_pk_f16_f32 v54, v52, v53
	ds_write_b64 v100, v[54:55] offset:53248
	s_add_u32 s80, s22, 0xa0b00
	s_addc_u32 s81, s90, 0
	s_add_u32 s100, s22, 0x60b00
	s_addc_u32 s101, s90, 0
	global_load_dwordx4 v[44:47], v201, s[100:101] nt
	s_setprio 1
	s_waitcnt lgkmcnt(1)
	v_mfma_f32_16x16x32_f16 v[80:83], v[234:237], v[210:213], v[80:83]
	v_mfma_f32_16x16x32_f16 v[120:123], v[234:237], v[218:221], v[120:123]
	v_mfma_f32_16x16x32_f16 v[124:127], v[238:241], v[206:209], v[124:127]
	v_mfma_f32_16x16x32_f16 v[146:149], v[238:241], v[214:217], v[146:149]
	v_mfma_f32_16x16x32_f16 v[134:137], v[238:241], v[218:221], v[134:137]
	v_mfma_f32_16x16x32_f16 v[242:245], v[234:237], v[206:209], v[8:11]
	v_mfma_f32_16x16x32_f16 v[138:141], v[234:237], v[214:217], v[138:141]
	v_mfma_f32_16x16x32_f16 v[142:145], v[238:241], v[210:213], v[142:145]
	s_setprio 0
	ds_read_b128 v[8:11], v130 offset:8192
	ds_read_b128 v[234:237], v130 offset:10240
	v_cvt_pk_f16_f32 v59, v58, v59
	v_cvt_pk_f16_f32 v58, v56, v57
	ds_write_b64 v100, v[58:59] offset:57344
	s_add_u32 s80, s22, 0xc0b00
	s_addc_u32 s81, s90, 0
	s_add_u32 s100, s22, 0x80b00
	s_addc_u32 s101, s90, 0
	global_load_dwordx4 v[48:51], v201, s[100:101] nt
	s_add_u32 s100, s22, 0xa0b00
	s_addc_u32 s101, s90, 0
	global_load_dwordx4 v[52:55], v201, s[100:101] nt
	s_setprio 1
	s_waitcnt lgkmcnt(1)
	v_mfma_f32_16x16x32_f16 v[84:87], v[8:11], v[210:213], v[84:87]
	v_mfma_f32_16x16x32_f16 v[238:241], v[8:11], v[206:209], v[68:71]
	v_mfma_f32_16x16x32_f16 v[170:173], v[8:11], v[214:217], v[170:173]
	v_mfma_f32_16x16x32_f16 v[150:153], v[8:11], v[218:221], v[150:153]
	v_mfma_f32_16x16x32_f16 v[162:165], v[234:237], v[206:209], v[162:165]
	v_mfma_f32_16x16x32_f16 v[174:177], v[234:237], v[210:213], v[174:177]
	v_mfma_f32_16x16x32_f16 v[178:181], v[234:237], v[214:217], v[178:181]
	v_mfma_f32_16x16x32_f16 v[154:157], v[234:237], v[218:221], v[154:157]
	s_setprio 0
	ds_read_b128 v[8:11], v130 offset:12288
	ds_read_b128 v[68:71], v130 offset:14336
	v_cvt_pk_f16_f32 v63, v62, v63
	v_cvt_pk_f16_f32 v62, v60, v61
	ds_write_b64 v100, v[62:63] offset:61440
	s_add_u32 s80, s22, 0xe0b00
	s_addc_u32 s81, s90, 0
	s_add_u32 s100, s22, 0xc0b00
	s_addc_u32 s101, s90, 0
	global_load_dwordx4 v[56:59], v201, s[100:101] nt
	s_add_u32 s100, s22, 0xe0b00
	s_addc_u32 s101, s90, 0
	global_load_dwordx4 v[60:63], v201, s[100:101] nt
	s_setprio 1
	s_waitcnt lgkmcnt(1)
	v_mfma_f32_16x16x32_f16 v[88:91], v[8:11], v[210:213], v[88:91]
	v_mfma_f32_16x16x32_f16 v[234:237], v[8:11], v[206:209], v[72:75]
	v_mfma_f32_16x16x32_f16 v[158:161], v[8:11], v[214:217], v[158:161]
	v_mfma_f32_16x16x32_f16 v[166:169], v[8:11], v[218:221], v[166:169]
	v_mfma_f32_16x16x32_f16 v[182:185], v[68:71], v[206:209], v[182:185]
	v_mfma_f32_16x16x32_f16 v[190:193], v[68:71], v[210:213], v[190:193]
	v_mfma_f32_16x16x32_f16 v[202:205], v[68:71], v[214:217], v[202:205]
	v_mfma_f32_16x16x32_f16 v[186:189], v[68:71], v[218:221], v[186:189]
	s_setprio 0
	s_waitcnt vmcnt(7)
	s_waitcnt lgkmcnt(0)
	s_barrier
	ds_read_b128 v[206:209], v131 offset:32768
	ds_read_b128 v[210:213], v131 offset:34816
	ds_read_b128 v[214:217], v131 offset:36864
	ds_read_b128 v[218:221], v131 offset:38912
	ds_read_b128 v[68:71], v129 offset:32768
	ds_read_b128 v[72:75], v129 offset:34816
	s_add_u32 s80, s22, 0xc00
	v_lshl_add_u64 v[92:93], s[46:47], 0, v[196:197]
	s_addc_u32 s81, s90, 0
	v_readfirstlane_b32 s1, v94
	s_mov_b32 m0, s1
	v_cvt_pk_f16_f32 v3, v2, v3
	global_load_lds_dwordx4 v[92:93], off
	v_cvt_pk_f16_f32 v2, v0, v1
	ds_write_b64 v100, v[2:3]
	s_setprio 1
	s_waitcnt lgkmcnt(1)
	v_mfma_f32_16x16x32_f16 v[0:3], v[68:71], v[206:209], v[76:79]
	v_mfma_f32_16x16x32_f16 v[104:107], v[68:71], v[214:217], v[104:107]
	v_mfma_f32_16x16x32_f16 v[108:111], v[72:75], v[206:209], v[108:111]
	v_mfma_f32_16x16x32_f16 v[112:115], v[72:75], v[210:213], v[112:115]
	v_mfma_f32_16x16x32_f16 v[116:119], v[72:75], v[214:217], v[116:119]
	v_mfma_f32_16x16x32_f16 v[230:233], v[68:71], v[210:213], v[230:233]
	v_mfma_f32_16x16x32_f16 v[222:225], v[68:71], v[218:221], v[222:225]
	v_mfma_f32_16x16x32_f16 v[226:229], v[72:75], v[218:221], v[226:229]
	s_setprio 0
	ds_read_b128 v[72:75], v129 offset:36864
	ds_read_b128 v[76:79], v129 offset:38912
	v_readfirstlane_b32 s92, v99
	v_lshl_add_u64 v[68:69], v[92:93], 0, s[58:59]
	s_mov_b32 m0, s92
	v_cvt_pk_f16_f32 v15, v14, v15
	global_load_lds_dwordx4 v[68:69], off
	v_cvt_pk_f16_f32 v14, v12, v13
	ds_write_b64 v100, v[14:15] offset:4096
	s_add_u32 s80, s22, 0x20c00
	s_addc_u32 s81, s90, 0
	s_setprio 1
	s_waitcnt lgkmcnt(1)
	v_mfma_f32_16x16x32_f16 v[12:15], v[72:75], v[206:209], v[242:245]
	v_mfma_f32_16x16x32_f16 v[120:123], v[72:75], v[218:221], v[120:123]
	v_mfma_f32_16x16x32_f16 v[124:127], v[76:79], v[206:209], v[124:127]
	v_mfma_f32_16x16x32_f16 v[146:149], v[76:79], v[214:217], v[146:149]
	v_mfma_f32_16x16x32_f16 v[134:137], v[76:79], v[218:221], v[134:137]
	v_mfma_f32_16x16x32_f16 v[242:245], v[72:75], v[210:213], v[80:83]
	v_mfma_f32_16x16x32_f16 v[138:141], v[72:75], v[214:217], v[138:141]
	v_mfma_f32_16x16x32_f16 v[142:145], v[76:79], v[210:213], v[142:145]
	s_setprio 0
	ds_read_b128 v[76:79], v129 offset:40960
	ds_read_b128 v[80:83], v129 offset:43008
	v_readfirstlane_b32 s91, v101
	v_lshl_add_u64 v[72:73], v[92:93], 0, s[60:61]
	s_mov_b32 m0, s91
	v_cvt_pk_f16_f32 v19, v18, v19
	global_load_lds_dwordx4 v[72:73], off
	v_cvt_pk_f16_f32 v18, v16, v17
	ds_write_b64 v100, v[18:19] offset:8192
	s_add_u32 s80, s22, 0x40c00
	s_addc_u32 s81, s90, 0
	s_add_u32 s100, s22, 0xc00
	s_addc_u32 s101, s90, 0
	global_load_dwordx4 v[8:11], v201, s[100:101] nt
	s_setprio 1
	s_waitcnt lgkmcnt(1)
	v_mfma_f32_16x16x32_f16 v[16:19], v[76:79], v[206:209], v[238:241]
	v_mfma_f32_16x16x32_f16 v[238:241], v[76:79], v[210:213], v[84:87]
	v_mfma_f32_16x16x32_f16 v[170:173], v[76:79], v[214:217], v[170:173]
	v_mfma_f32_16x16x32_f16 v[150:153], v[76:79], v[218:221], v[150:153]
	v_mfma_f32_16x16x32_f16 v[162:165], v[80:83], v[206:209], v[162:165]
	v_mfma_f32_16x16x32_f16 v[174:177], v[80:83], v[210:213], v[174:177]
	v_mfma_f32_16x16x32_f16 v[178:181], v[80:83], v[214:217], v[178:181]
	v_mfma_f32_16x16x32_f16 v[154:157], v[80:83], v[218:221], v[154:157]
	s_setprio 0
	ds_read_b128 v[80:83], v129 offset:45056
	ds_read_b128 v[84:87], v129 offset:47104
	v_readfirstlane_b32 s73, v102
	v_lshl_add_u64 v[76:77], v[92:93], 0, s[62:63]
	s_mov_b32 m0, s73
	v_cvt_pk_f16_f32 v23, v22, v23
	global_load_lds_dwordx4 v[76:77], off
	v_cvt_pk_f16_f32 v22, v20, v21
	ds_write_b64 v100, v[22:23] offset:12288
	s_add_u32 s80, s22, 0x60c00
	s_addc_u32 s81, s90, 0
	s_add_u32 s100, s22, 0x20c00
	s_addc_u32 s101, s90, 0
	global_load_dwordx4 v[68:71], v201, s[100:101] nt
	s_setprio 1
	s_waitcnt lgkmcnt(1)
	v_mfma_f32_16x16x32_f16 v[20:23], v[80:83], v[206:209], v[234:237]
	v_mfma_f32_16x16x32_f16 v[234:237], v[80:83], v[210:213], v[88:91]
	v_mfma_f32_16x16x32_f16 v[158:161], v[80:83], v[214:217], v[158:161]
	v_mfma_f32_16x16x32_f16 v[166:169], v[80:83], v[218:221], v[166:169]
	v_mfma_f32_16x16x32_f16 v[182:185], v[84:87], v[206:209], v[182:185]
	v_mfma_f32_16x16x32_f16 v[190:193], v[84:87], v[210:213], v[190:193]
	v_mfma_f32_16x16x32_f16 v[202:205], v[84:87], v[214:217], v[202:205]
	v_mfma_f32_16x16x32_f16 v[186:189], v[84:87], v[218:221], v[186:189]
	s_setprio 0
	ds_read_b128 v[206:209], v128 offset:32768
	ds_read_b128 v[210:213], v128 offset:34816
	ds_read_b128 v[214:217], v128 offset:36864
	ds_read_b128 v[218:221], v128 offset:38912
	ds_read_b128 v[84:87], v130 offset:32768
	ds_read_b128 v[88:91], v130 offset:34816
	v_cvt_pk_f16_f32 v27, v26, v27
	v_cvt_pk_f16_f32 v26, v24, v25
	ds_write_b64 v100, v[26:27] offset:16384
	s_add_u32 s80, s22, 0x80c00
	s_addc_u32 s81, s90, 0
	s_add_u32 s100, s22, 0x40c00
	s_addc_u32 s101, s90, 0
	global_load_dwordx4 v[72:75], v201, s[100:101] nt
	s_setprio 1
	s_waitcnt lgkmcnt(1)
	v_mfma_f32_16x16x32_f16 v[24:27], v[84:87], v[206:209], v[0:3]
	v_mfma_f32_16x16x32_f16 v[104:107], v[84:87], v[214:217], v[104:107]
	v_mfma_f32_16x16x32_f16 v[108:111], v[88:91], v[206:209], v[108:111]
	v_mfma_f32_16x16x32_f16 v[112:115], v[88:91], v[210:213], v[112:115]
	v_mfma_f32_16x16x32_f16 v[116:119], v[88:91], v[214:217], v[116:119]
	v_mfma_f32_16x16x32_f16 v[230:233], v[84:87], v[210:213], v[230:233]
	v_mfma_f32_16x16x32_f16 v[222:225], v[84:87], v[218:221], v[222:225]
	v_mfma_f32_16x16x32_f16 v[226:229], v[88:91], v[218:221], v[226:229]
	s_setprio 0
	ds_read_b128 v[0:3], v130 offset:36864
	ds_read_b128 v[88:91], v130 offset:38912
	v_cvt_pk_f16_f32 v31, v30, v31
	v_cvt_pk_f16_f32 v30, v28, v29
	ds_write_b64 v100, v[30:31] offset:20480
	s_add_u32 s80, s22, 0xa0c00
	s_addc_u32 s81, s90, 0
	s_add_u32 s100, s22, 0x60c00
	s_addc_u32 s101, s90, 0
	global_load_dwordx4 v[76:79], v201, s[100:101] nt
	s_setprio 1
	s_waitcnt lgkmcnt(1)
	v_mfma_f32_16x16x32_f16 v[12:15], v[0:3], v[206:209], v[12:15]
	v_mfma_f32_16x16x32_f16 v[28:31], v[0:3], v[210:213], v[242:245]
	v_mfma_f32_16x16x32_f16 v[120:123], v[0:3], v[218:221], v[120:123]
	v_mfma_f32_16x16x32_f16 v[124:127], v[88:91], v[206:209], v[124:127]
	v_mfma_f32_16x16x32_f16 v[146:149], v[88:91], v[214:217], v[146:149]
	v_mfma_f32_16x16x32_f16 v[134:137], v[88:91], v[218:221], v[134:137]
	v_mfma_f32_16x16x32_f16 v[138:141], v[0:3], v[214:217], v[138:141]
	v_mfma_f32_16x16x32_f16 v[142:145], v[88:91], v[210:213], v[142:145]
	s_setprio 0
	ds_read_b128 v[0:3], v130 offset:40960
	ds_read_b128 v[242:245], v130 offset:43008
	v_cvt_pk_f16_f32 v35, v34, v35
	v_cvt_pk_f16_f32 v34, v32, v33
	ds_write_b64 v100, v[34:35] offset:24576
	s_add_u32 s80, s22, 0xc0c00
	s_addc_u32 s81, s90, 0
	s_add_u32 s100, s22, 0x80c00
	s_addc_u32 s101, s90, 0
	global_load_dwordx4 v[80:83], v201, s[100:101] nt
	s_add_u32 s100, s22, 0xa0c00
	s_addc_u32 s101, s90, 0
	global_load_dwordx4 v[84:87], v201, s[100:101] nt
	s_setprio 1
	s_waitcnt lgkmcnt(1)
	v_mfma_f32_16x16x32_f16 v[16:19], v[0:3], v[206:209], v[16:19]
	v_mfma_f32_16x16x32_f16 v[32:35], v[0:3], v[210:213], v[238:241]
	v_mfma_f32_16x16x32_f16 v[170:173], v[0:3], v[214:217], v[170:173]
	v_mfma_f32_16x16x32_f16 v[150:153], v[0:3], v[218:221], v[150:153]
	v_mfma_f32_16x16x32_f16 v[162:165], v[242:245], v[206:209], v[162:165]
	v_mfma_f32_16x16x32_f16 v[174:177], v[242:245], v[210:213], v[174:177]
	v_mfma_f32_16x16x32_f16 v[178:181], v[242:245], v[214:217], v[178:181]
	v_mfma_f32_16x16x32_f16 v[154:157], v[242:245], v[218:221], v[154:157]
	s_setprio 0
	ds_read_b128 v[0:3], v130 offset:45056
	ds_read_b128 v[238:241], v130 offset:47104
	v_cvt_pk_f16_f32 v39, v38, v39
	v_cvt_pk_f16_f32 v38, v36, v37
	ds_write_b64 v100, v[38:39] offset:28672
	s_add_u32 s80, s22, 0xe0c00
	s_addc_u32 s81, s90, 0
	s_add_u32 s100, s22, 0xc0c00
	s_addc_u32 s101, s90, 0
	global_load_dwordx4 v[88:91], v201, s[100:101] nt
	s_add_u32 s100, s22, 0xe0c00
	s_addc_u32 s101, s90, 0
	global_load_dwordx4 v[36:39], v201, s[100:101] nt
	s_setprio 1
	s_waitcnt lgkmcnt(1)
	v_mfma_f32_16x16x32_f16 v[20:23], v[0:3], v[206:209], v[20:23]
	v_mfma_f32_16x16x32_f16 v[234:237], v[0:3], v[210:213], v[234:237]
	v_mfma_f32_16x16x32_f16 v[158:161], v[0:3], v[214:217], v[158:161]
	v_mfma_f32_16x16x32_f16 v[166:169], v[0:3], v[218:221], v[166:169]
	v_mfma_f32_16x16x32_f16 v[182:185], v[238:241], v[206:209], v[182:185]
	v_mfma_f32_16x16x32_f16 v[190:193], v[238:241], v[210:213], v[190:193]
	v_mfma_f32_16x16x32_f16 v[202:205], v[238:241], v[214:217], v[202:205]
	v_mfma_f32_16x16x32_f16 v[186:189], v[238:241], v[218:221], v[186:189]
	s_setprio 0
	s_waitcnt vmcnt(7)
	s_waitcnt lgkmcnt(0)
	s_barrier
	ds_read_b128 v[206:209], v131
	ds_read_b128 v[210:213], v131 offset:2048
	ds_read_b128 v[214:217], v131 offset:4096
	ds_read_b128 v[218:221], v131 offset:6144
	ds_read_b128 v[238:241], v129
	ds_read_b128 v[242:245], v129 offset:2048
	s_add_u32 s80, s22, 0xd00
	v_lshl_add_u64 v[92:93], s[48:49], 0, v[196:197]
	s_addc_u32 s81, s90, 0
	s_mov_b32 m0, s0
	v_cvt_pk_f16_f32 v1, v6, v7
	global_load_lds_dwordx4 v[92:93], off
	v_cvt_pk_f16_f32 v0, v4, v5
	ds_write_b64 v100, v[0:1] offset:32768
	s_setprio 1
	s_waitcnt lgkmcnt(1)
	v_mfma_f32_16x16x32_f16 v[24:27], v[238:241], v[206:209], v[24:27]
	v_mfma_f32_16x16x32_f16 v[104:107], v[238:241], v[214:217], v[104:107]
	v_mfma_f32_16x16x32_f16 v[108:111], v[242:245], v[206:209], v[108:111]
	v_mfma_f32_16x16x32_f16 v[112:115], v[242:245], v[210:213], v[112:115]
	v_mfma_f32_16x16x32_f16 v[116:119], v[242:245], v[214:217], v[116:119]
	v_mfma_f32_16x16x32_f16 v[230:233], v[238:241], v[210:213], v[230:233]
	v_mfma_f32_16x16x32_f16 v[222:225], v[238:241], v[218:221], v[222:225]
	v_mfma_f32_16x16x32_f16 v[226:229], v[242:245], v[218:221], v[226:229]
	s_setprio 0
	ds_read_b128 v[238:241], v129 offset:4096
	ds_read_b128 v[242:245], v129 offset:6144
	s_mov_b32 m0, s72
	v_lshl_add_u64 v[4:5], v[92:93], 0, s[58:59]
	global_load_lds_dwordx4 v[4:5], off
	v_cvt_pk_f16_f32 v5, v66, v67
	v_cvt_pk_f16_f32 v4, v64, v65
	ds_write_b64 v100, v[4:5] offset:36864
	s_add_u32 s80, s22, 0x20d00
	s_addc_u32 s81, s90, 0
	s_setprio 1
	s_waitcnt lgkmcnt(1)
	v_mfma_f32_16x16x32_f16 v[64:67], v[238:241], v[206:209], v[12:15]
	v_mfma_f32_16x16x32_f16 v[28:31], v[238:241], v[210:213], v[28:31]
	v_mfma_f32_16x16x32_f16 v[120:123], v[238:241], v[218:221], v[120:123]
	v_mfma_f32_16x16x32_f16 v[124:127], v[242:245], v[206:209], v[124:127]
	v_mfma_f32_16x16x32_f16 v[146:149], v[242:245], v[214:217], v[146:149]
	v_mfma_f32_16x16x32_f16 v[134:137], v[242:245], v[218:221], v[134:137]
	v_mfma_f32_16x16x32_f16 v[138:141], v[238:241], v[214:217], v[138:141]
	v_mfma_f32_16x16x32_f16 v[142:145], v[242:245], v[210:213], v[142:145]
	s_setprio 0
	ds_read_b128 v[238:241], v129 offset:8192
	ds_read_b128 v[242:245], v129 offset:10240
	s_mov_b32 m0, s71
	v_lshl_add_u64 v[12:13], v[92:93], 0, s[60:61]
	global_load_lds_dwordx4 v[12:13], off
	v_cvt_pk_f16_f32 v13, v42, v43
	v_cvt_pk_f16_f32 v12, v40, v41
	ds_write_b64 v100, v[12:13] offset:40960
	s_add_u32 s80, s22, 0x40d00
	s_addc_u32 s81, s90, 0
	s_add_u32 s100, s22, 0xd00
	s_addc_u32 s101, s90, 0
	global_load_dwordx4 v[0:3], v201, s[100:101] nt
	s_setprio 1
	s_waitcnt lgkmcnt(1)
	v_mfma_f32_16x16x32_f16 v[40:43], v[238:241], v[206:209], v[16:19]
	v_mfma_f32_16x16x32_f16 v[32:35], v[238:241], v[210:213], v[32:35]
	v_mfma_f32_16x16x32_f16 v[170:173], v[238:241], v[214:217], v[170:173]
	v_mfma_f32_16x16x32_f16 v[150:153], v[238:241], v[218:221], v[150:153]
	v_mfma_f32_16x16x32_f16 v[162:165], v[242:245], v[206:209], v[162:165]
	v_mfma_f32_16x16x32_f16 v[174:177], v[242:245], v[210:213], v[174:177]
	v_mfma_f32_16x16x32_f16 v[178:181], v[242:245], v[214:217], v[178:181]
	v_mfma_f32_16x16x32_f16 v[154:157], v[242:245], v[218:221], v[154:157]
	s_setprio 0
	ds_read_b128 v[238:241], v129 offset:12288
	ds_read_b128 v[242:245], v129 offset:14336
	s_mov_b32 m0, s70
	v_lshl_add_u64 v[16:17], v[92:93], 0, s[62:63]
	global_load_lds_dwordx4 v[16:17], off
	v_cvt_pk_f16_f32 v17, v46, v47
	v_cvt_pk_f16_f32 v16, v44, v45
	ds_write_b64 v100, v[16:17] offset:45056
	s_add_u32 s70, s22, 0x60d00
	s_addc_u32 s71, s90, 0
	s_add_u32 s100, s22, 0x20d00
	s_addc_u32 s101, s90, 0
	global_load_dwordx4 v[4:7], v201, s[100:101] nt
	s_setprio 1
	s_waitcnt lgkmcnt(1)
	v_mfma_f32_16x16x32_f16 v[44:47], v[238:241], v[206:209], v[20:23]
	v_mfma_f32_16x16x32_f16 v[234:237], v[238:241], v[210:213], v[234:237]
	v_mfma_f32_16x16x32_f16 v[158:161], v[238:241], v[214:217], v[158:161]
	v_mfma_f32_16x16x32_f16 v[166:169], v[238:241], v[218:221], v[166:169]
	v_mfma_f32_16x16x32_f16 v[182:185], v[242:245], v[206:209], v[182:185]
	v_mfma_f32_16x16x32_f16 v[190:193], v[242:245], v[210:213], v[190:193]
	v_mfma_f32_16x16x32_f16 v[202:205], v[242:245], v[214:217], v[202:205]
	v_mfma_f32_16x16x32_f16 v[186:189], v[242:245], v[218:221], v[186:189]
	s_setprio 0
	ds_read_b128 v[206:209], v128
	ds_read_b128 v[210:213], v128 offset:2048
	ds_read_b128 v[214:217], v128 offset:4096
	ds_read_b128 v[218:221], v128 offset:6144
	ds_read_b128 v[238:241], v130
	ds_read_b128 v[242:245], v130 offset:2048
	v_cvt_pk_f16_f32 v21, v50, v51
	v_cvt_pk_f16_f32 v20, v48, v49
	ds_write_b64 v100, v[20:21] offset:49152
	s_add_u32 s70, s22, 0x80d00
	s_addc_u32 s71, s90, 0
	s_add_u32 s100, s22, 0x40d00
	s_addc_u32 s101, s90, 0
	global_load_dwordx4 v[12:15], v201, s[100:101] nt
	s_setprio 1
	s_waitcnt lgkmcnt(1)
	v_mfma_f32_16x16x32_f16 v[48:51], v[238:241], v[206:209], v[24:27]
	v_mfma_f32_16x16x32_f16 v[104:107], v[238:241], v[214:217], v[104:107]
	v_mfma_f32_16x16x32_f16 v[108:111], v[242:245], v[206:209], v[108:111]
	v_mfma_f32_16x16x32_f16 v[112:115], v[242:245], v[210:213], v[112:115]
	v_mfma_f32_16x16x32_f16 v[116:119], v[242:245], v[214:217], v[116:119]
	v_mfma_f32_16x16x32_f16 v[230:233], v[238:241], v[210:213], v[230:233]
	v_mfma_f32_16x16x32_f16 v[222:225], v[238:241], v[218:221], v[222:225]
	v_mfma_f32_16x16x32_f16 v[226:229], v[242:245], v[218:221], v[226:229]
	s_setprio 0
	ds_read_b128 v[238:241], v130 offset:4096
	ds_read_b128 v[242:245], v130 offset:6144
	v_cvt_pk_f16_f32 v25, v54, v55
	v_cvt_pk_f16_f32 v24, v52, v53
	ds_write_b64 v100, v[24:25] offset:53248
	s_add_u32 s70, s22, 0xa0d00
	s_addc_u32 s71, s90, 0
	s_add_u32 s100, s22, 0x60d00
	s_addc_u32 s101, s90, 0
	global_load_dwordx4 v[16:19], v201, s[100:101] nt
	s_setprio 1
	s_waitcnt lgkmcnt(1)
	v_mfma_f32_16x16x32_f16 v[52:55], v[238:241], v[206:209], v[64:67]
	v_mfma_f32_16x16x32_f16 v[64:67], v[238:241], v[210:213], v[28:31]
	v_mfma_f32_16x16x32_f16 v[120:123], v[238:241], v[218:221], v[120:123]
	v_mfma_f32_16x16x32_f16 v[124:127], v[242:245], v[206:209], v[124:127]
	v_mfma_f32_16x16x32_f16 v[146:149], v[242:245], v[214:217], v[146:149]
	v_mfma_f32_16x16x32_f16 v[134:137], v[242:245], v[218:221], v[134:137]
	v_mfma_f32_16x16x32_f16 v[138:141], v[238:241], v[214:217], v[138:141]
	v_mfma_f32_16x16x32_f16 v[142:145], v[242:245], v[210:213], v[142:145]
	s_setprio 0
	ds_read_b128 v[238:241], v130 offset:8192
	ds_read_b128 v[242:245], v130 offset:10240
	v_cvt_pk_f16_f32 v29, v58, v59
	v_cvt_pk_f16_f32 v28, v56, v57
	ds_write_b64 v100, v[28:29] offset:57344
	s_add_u32 s70, s22, 0xc0d00
	s_addc_u32 s71, s90, 0
	s_add_u32 s100, s22, 0x80d00
	s_addc_u32 s101, s90, 0
	global_load_dwordx4 v[20:23], v201, s[100:101] nt
	s_add_u32 s100, s22, 0xa0d00
	s_addc_u32 s101, s90, 0
	global_load_dwordx4 v[24:27], v201, s[100:101] nt
	s_setprio 1
	s_waitcnt lgkmcnt(1)
	v_mfma_f32_16x16x32_f16 v[56:59], v[238:241], v[206:209], v[40:43]
	v_mfma_f32_16x16x32_f16 v[246:249], v[238:241], v[210:213], v[32:35]
	v_mfma_f32_16x16x32_f16 v[170:173], v[238:241], v[214:217], v[170:173]
	v_mfma_f32_16x16x32_f16 v[150:153], v[238:241], v[218:221], v[150:153]
	v_mfma_f32_16x16x32_f16 v[162:165], v[242:245], v[206:209], v[162:165]
	v_mfma_f32_16x16x32_f16 v[174:177], v[242:245], v[210:213], v[174:177]
	v_mfma_f32_16x16x32_f16 v[178:181], v[242:245], v[214:217], v[178:181]
	v_mfma_f32_16x16x32_f16 v[154:157], v[242:245], v[218:221], v[154:157]
	s_setprio 0
	ds_read_b128 v[40:43], v130 offset:12288
	ds_read_b128 v[238:241], v130 offset:14336
	v_cvt_pk_f16_f32 v33, v62, v63
	v_cvt_pk_f16_f32 v32, v60, v61
	ds_write_b64 v100, v[32:33] offset:61440
	s_add_u32 s70, s22, 0xe0d00
	s_addc_u32 s71, s90, 0
	s_add_u32 s100, s22, 0xc0d00
	s_addc_u32 s101, s90, 0
	global_load_dwordx4 v[28:31], v201, s[100:101] nt
	s_add_u32 s100, s22, 0xe0d00
	s_addc_u32 s101, s90, 0
	global_load_dwordx4 v[32:35], v201, s[100:101] nt
	s_setprio 1
	s_waitcnt lgkmcnt(1)
	v_mfma_f32_16x16x32_f16 v[60:63], v[40:43], v[206:209], v[44:47]
	v_mfma_f32_16x16x32_f16 v[234:237], v[40:43], v[210:213], v[234:237]
	v_mfma_f32_16x16x32_f16 v[158:161], v[40:43], v[214:217], v[158:161]
	v_mfma_f32_16x16x32_f16 v[166:169], v[40:43], v[218:221], v[166:169]
	v_mfma_f32_16x16x32_f16 v[182:185], v[238:241], v[206:209], v[182:185]
	v_mfma_f32_16x16x32_f16 v[190:193], v[238:241], v[210:213], v[190:193]
	v_mfma_f32_16x16x32_f16 v[202:205], v[238:241], v[214:217], v[202:205]
	v_mfma_f32_16x16x32_f16 v[186:189], v[238:241], v[218:221], v[186:189]
	s_setprio 0
	s_waitcnt vmcnt(7)
	s_waitcnt lgkmcnt(0)
	s_barrier
	ds_read_b128 v[206:209], v131 offset:32768
	ds_read_b128 v[210:213], v131 offset:34816
	ds_read_b128 v[214:217], v131 offset:36864
	ds_read_b128 v[218:221], v131 offset:38912
	ds_read_b128 v[40:43], v129 offset:32768
	ds_read_b128 v[44:47], v129 offset:34816
	s_add_u32 s70, s22, 0xe00
	v_lshl_add_u64 v[92:93], s[50:51], 0, v[196:197]
	s_addc_u32 s71, s90, 0
	s_mov_b32 m0, s1
	v_cvt_pk_f16_f32 v11, v10, v11
	global_load_lds_dwordx4 v[92:93], off
	v_cvt_pk_f16_f32 v10, v8, v9
	ds_write_b64 v100, v[10:11]
	s_setprio 1
	s_waitcnt lgkmcnt(1)
	v_mfma_f32_16x16x32_f16 v[104:107], v[40:43], v[214:217], v[104:107]
	v_mfma_f32_16x16x32_f16 v[108:111], v[44:47], v[206:209], v[108:111]
	v_mfma_f32_16x16x32_f16 v[112:115], v[44:47], v[210:213], v[112:115]
	v_mfma_f32_16x16x32_f16 v[116:119], v[44:47], v[214:217], v[116:119]
	v_mfma_f32_16x16x32_f16 v[238:241], v[40:43], v[206:209], v[48:51]
	v_mfma_f32_16x16x32_f16 v[230:233], v[40:43], v[210:213], v[230:233]
	v_mfma_f32_16x16x32_f16 v[222:225], v[40:43], v[218:221], v[222:225]
	v_mfma_f32_16x16x32_f16 v[226:229], v[44:47], v[218:221], v[226:229]
	s_setprio 0
	ds_read_b128 v[44:47], v129 offset:36864
	ds_read_b128 v[48:51], v129 offset:38912
	s_mov_b32 m0, s92
	v_lshl_add_u64 v[40:41], v[92:93], 0, s[58:59]
	global_load_lds_dwordx4 v[40:41], off
	v_cvt_pk_f16_f32 v41, v70, v71
	v_cvt_pk_f16_f32 v40, v68, v69
	ds_write_b64 v100, v[40:41] offset:4096
	s_add_u32 s0, s22, 0x20e00
	s_addc_u32 s1, s90, 0
	s_setprio 1
	s_waitcnt lgkmcnt(1)
	v_mfma_f32_16x16x32_f16 v[68:71], v[44:47], v[206:209], v[52:55]
	v_mfma_f32_16x16x32_f16 v[64:67], v[44:47], v[210:213], v[64:67]
	v_mfma_f32_16x16x32_f16 v[120:123], v[44:47], v[218:221], v[120:123]
	v_mfma_f32_16x16x32_f16 v[124:127], v[48:51], v[206:209], v[124:127]
	v_mfma_f32_16x16x32_f16 v[146:149], v[48:51], v[214:217], v[146:149]
	v_mfma_f32_16x16x32_f16 v[134:137], v[48:51], v[218:221], v[134:137]
	v_mfma_f32_16x16x32_f16 v[138:141], v[44:47], v[214:217], v[138:141]
	v_mfma_f32_16x16x32_f16 v[142:145], v[48:51], v[210:213], v[142:145]
	s_setprio 0
	ds_read_b128 v[48:51], v129 offset:40960
	ds_read_b128 v[52:55], v129 offset:43008
	s_mov_b32 m0, s91
	v_lshl_add_u64 v[44:45], v[92:93], 0, s[60:61]
	global_load_lds_dwordx4 v[44:45], off
	v_cvt_pk_f16_f32 v45, v74, v75
	v_cvt_pk_f16_f32 v44, v72, v73
	ds_write_b64 v100, v[44:45] offset:8192
	s_add_u32 s0, s22, 0x40e00
	s_addc_u32 s1, s90, 0
	s_add_u32 s100, s22, 0xe00
	s_addc_u32 s101, s90, 0
	global_load_dwordx4 v[8:11], v201, s[100:101] nt
	s_setprio 1
	s_waitcnt lgkmcnt(1)
	v_mfma_f32_16x16x32_f16 v[72:75], v[48:51], v[206:209], v[56:59]
	v_mfma_f32_16x16x32_f16 v[242:245], v[48:51], v[210:213], v[246:249]
	v_mfma_f32_16x16x32_f16 v[170:173], v[48:51], v[214:217], v[170:173]
	v_mfma_f32_16x16x32_f16 v[150:153], v[48:51], v[218:221], v[150:153]
	v_mfma_f32_16x16x32_f16 v[162:165], v[52:55], v[206:209], v[162:165]
	v_mfma_f32_16x16x32_f16 v[174:177], v[52:55], v[210:213], v[174:177]
	v_mfma_f32_16x16x32_f16 v[178:181], v[52:55], v[214:217], v[178:181]
	v_mfma_f32_16x16x32_f16 v[154:157], v[52:55], v[218:221], v[154:157]
	s_setprio 0
	ds_read_b128 v[52:55], v129 offset:45056
	ds_read_b128 v[56:59], v129 offset:47104
	s_mov_b32 m0, s73
	v_lshl_add_u64 v[48:49], v[92:93], 0, s[62:63]
	global_load_lds_dwordx4 v[48:49], off
	v_cvt_pk_f16_f32 v49, v78, v79
	v_cvt_pk_f16_f32 v48, v76, v77
	ds_write_b64 v100, v[48:49] offset:12288
	s_add_u32 s0, s22, 0x60e00
	s_addc_u32 s1, s90, 0
	s_add_u32 s100, s22, 0x20e00
	s_addc_u32 s101, s90, 0
	global_load_dwordx4 v[40:43], v201, s[100:101] nt
	s_setprio 1
	s_waitcnt lgkmcnt(1)
	v_mfma_f32_16x16x32_f16 v[76:79], v[52:55], v[206:209], v[60:63]
	v_mfma_f32_16x16x32_f16 v[234:237], v[52:55], v[210:213], v[234:237]
	v_mfma_f32_16x16x32_f16 v[158:161], v[52:55], v[214:217], v[158:161]
	v_mfma_f32_16x16x32_f16 v[166:169], v[52:55], v[218:221], v[166:169]
	v_mfma_f32_16x16x32_f16 v[182:185], v[56:59], v[206:209], v[182:185]
	v_mfma_f32_16x16x32_f16 v[190:193], v[56:59], v[210:213], v[190:193]
	v_mfma_f32_16x16x32_f16 v[202:205], v[56:59], v[214:217], v[202:205]
	v_mfma_f32_16x16x32_f16 v[186:189], v[56:59], v[218:221], v[186:189]
	s_setprio 0
	ds_read_b128 v[206:209], v128 offset:32768
	ds_read_b128 v[210:213], v128 offset:34816
	ds_read_b128 v[214:217], v128 offset:36864
	ds_read_b128 v[218:221], v128 offset:38912
	ds_read_b128 v[56:59], v130 offset:32768
	ds_read_b128 v[60:63], v130 offset:34816
	v_cvt_pk_f16_f32 v53, v82, v83
	v_cvt_pk_f16_f32 v52, v80, v81
	ds_write_b64 v100, v[52:53] offset:16384
	s_add_u32 s0, s22, 0x80e00
	s_addc_u32 s1, s90, 0
	s_add_u32 s100, s22, 0x40e00
	s_addc_u32 s101, s90, 0
	global_load_dwordx4 v[44:47], v201, s[100:101] nt
	s_setprio 1
	s_waitcnt lgkmcnt(1)
	v_mfma_f32_16x16x32_f16 v[80:83], v[56:59], v[206:209], v[238:241]
	v_mfma_f32_16x16x32_f16 v[104:107], v[56:59], v[214:217], v[104:107]
	v_mfma_f32_16x16x32_f16 v[108:111], v[60:63], v[206:209], v[108:111]
	v_mfma_f32_16x16x32_f16 v[112:115], v[60:63], v[210:213], v[112:115]
	v_mfma_f32_16x16x32_f16 v[116:119], v[60:63], v[214:217], v[116:119]
	v_mfma_f32_16x16x32_f16 v[230:233], v[56:59], v[210:213], v[230:233]
	v_mfma_f32_16x16x32_f16 v[222:225], v[56:59], v[218:221], v[222:225]
	v_mfma_f32_16x16x32_f16 v[226:229], v[60:63], v[218:221], v[226:229]
	s_setprio 0
	ds_read_b128 v[60:63], v130 offset:36864
	ds_read_b128 v[238:241], v130 offset:38912
	v_cvt_pk_f16_f32 v57, v86, v87
	v_cvt_pk_f16_f32 v56, v84, v85
	ds_write_b64 v100, v[56:57] offset:20480
	s_add_u32 s0, s22, 0xa0e00
	s_addc_u32 s1, s90, 0
	s_add_u32 s100, s22, 0x60e00
	s_addc_u32 s101, s90, 0
	global_load_dwordx4 v[48:51], v201, s[100:101] nt
	s_setprio 1
	s_waitcnt lgkmcnt(1)
	v_mfma_f32_16x16x32_f16 v[68:71], v[60:63], v[206:209], v[68:71]
	v_mfma_f32_16x16x32_f16 v[64:67], v[60:63], v[210:213], v[64:67]
	v_mfma_f32_16x16x32_f16 v[84:87], v[60:63], v[214:217], v[138:141]
	v_mfma_f32_16x16x32_f16 v[120:123], v[60:63], v[218:221], v[120:123]
	v_mfma_f32_16x16x32_f16 v[124:127], v[238:241], v[206:209], v[124:127]
	v_mfma_f32_16x16x32_f16 v[134:137], v[238:241], v[218:221], v[134:137]
	v_mfma_f32_16x16x32_f16 v[138:141], v[238:241], v[210:213], v[142:145]
	v_mfma_f32_16x16x32_f16 v[142:145], v[238:241], v[214:217], v[146:149]
	s_setprio 0
	s_nop 1
	ds_read_b128 v[146:149], v130 offset:40960
	ds_read_b128 v[238:241], v130 offset:43008
	v_cvt_pk_f16_f32 v61, v90, v91
	v_cvt_pk_f16_f32 v60, v88, v89
	ds_write_b64 v100, v[60:61] offset:24576
	s_add_u32 s0, s22, 0xc0e00
	s_addc_u32 s1, s90, 0
	s_add_u32 s100, s22, 0x80e00
	s_addc_u32 s101, s90, 0
	global_load_dwordx4 v[52:55], v201, s[100:101] nt
	s_add_u32 s100, s22, 0xa0e00
	s_addc_u32 s101, s90, 0
	global_load_dwordx4 v[56:59], v201, s[100:101] nt
	s_setprio 1
	s_waitcnt lgkmcnt(1)
	v_mfma_f32_16x16x32_f16 v[72:75], v[146:149], v[206:209], v[72:75]
	v_mfma_f32_16x16x32_f16 v[88:91], v[146:149], v[210:213], v[242:245]
	v_mfma_f32_16x16x32_f16 v[170:173], v[146:149], v[214:217], v[170:173]
	v_mfma_f32_16x16x32_f16 v[146:149], v[146:149], v[218:221], v[150:153]
	v_mfma_f32_16x16x32_f16 v[150:153], v[238:241], v[206:209], v[162:165]
	v_mfma_f32_16x16x32_f16 v[162:165], v[238:241], v[210:213], v[174:177]
	v_mfma_f32_16x16x32_f16 v[174:177], v[238:241], v[214:217], v[178:181]
	v_mfma_f32_16x16x32_f16 v[154:157], v[238:241], v[218:221], v[154:157]
	s_setprio 0
	s_nop 0
	ds_read_b128 v[178:181], v130 offset:45056
	ds_read_b128 v[238:241], v130 offset:47104
	v_cvt_pk_f16_f32 v39, v38, v39
	v_cvt_pk_f16_f32 v38, v36, v37
	ds_write_b64 v100, v[38:39] offset:28672
	s_add_u32 s0, s22, 0xe0e00
	s_addc_u32 s1, s90, 0
	s_add_u32 s100, s22, 0xc0e00
	s_addc_u32 s101, s90, 0
	global_load_dwordx4 v[60:63], v201, s[100:101] nt
	s_add_u32 s100, s22, 0xe0e00
	s_addc_u32 s101, s90, 0
	global_load_dwordx4 v[36:39], v201, s[100:101] nt
	s_setprio 1
	s_waitcnt lgkmcnt(1)
	v_mfma_f32_16x16x32_f16 v[76:79], v[178:181], v[206:209], v[76:79]
	v_mfma_f32_16x16x32_f16 v[234:237], v[178:181], v[210:213], v[234:237]
	v_mfma_f32_16x16x32_f16 v[158:161], v[178:181], v[214:217], v[158:161]
	v_mfma_f32_16x16x32_f16 v[166:169], v[178:181], v[218:221], v[166:169]
	v_mfma_f32_16x16x32_f16 v[178:181], v[238:241], v[206:209], v[182:185]
	v_mfma_f32_16x16x32_f16 v[182:185], v[238:241], v[210:213], v[190:193]
	v_mfma_f32_16x16x32_f16 v[190:193], v[238:241], v[214:217], v[202:205]
	v_mfma_f32_16x16x32_f16 v[186:189], v[238:241], v[218:221], v[186:189]
	s_setprio 0
	s_waitcnt vmcnt(7)
	s_waitcnt lgkmcnt(0)
	s_barrier
	ds_read_b128 v[202:205], v131
	ds_read_b128 v[206:209], v131 offset:2048
	ds_read_b128 v[210:213], v131 offset:4096
	ds_read_b128 v[214:217], v131 offset:6144
	ds_read_b128 v[218:221], v129
	ds_read_b128 v[238:241], v129 offset:2048
	s_add_u32 s70, s22, 0xf00
	v_lshl_add_u64 v[92:93], s[52:53], 0, v[196:197]
	s_addc_u32 s71, s90, 0
	v_readfirstlane_b32 s0, v95
	s_mov_b32 m0, s0
	v_cvt_pk_f16_f32 v3, v2, v3
	global_load_lds_dwordx4 v[92:93], off
	v_cvt_pk_f16_f32 v2, v0, v1
	ds_write_b64 v100, v[2:3] offset:32768
	s_setprio 1
	s_waitcnt lgkmcnt(1)
	v_mfma_f32_16x16x32_f16 v[80:83], v[218:221], v[202:205], v[80:83]
	v_mfma_f32_16x16x32_f16 v[104:107], v[218:221], v[210:213], v[104:107]
	v_mfma_f32_16x16x32_f16 v[108:111], v[238:241], v[202:205], v[108:111]
	v_mfma_f32_16x16x32_f16 v[112:115], v[238:241], v[206:209], v[112:115]
	v_mfma_f32_16x16x32_f16 v[116:119], v[238:241], v[210:213], v[116:119]
	v_mfma_f32_16x16x32_f16 v[230:233], v[218:221], v[206:209], v[230:233]
	v_mfma_f32_16x16x32_f16 v[218:221], v[218:221], v[214:217], v[222:225]
	v_mfma_f32_16x16x32_f16 v[222:225], v[238:241], v[214:217], v[226:229]
	s_setprio 0
	s_nop 1
	ds_read_b128 v[226:229], v129 offset:4096
	ds_read_b128 v[238:241], v129 offset:6144
	v_readfirstlane_b32 s1, v96
	v_lshl_add_u64 v[198:199], v[92:93], 0, s[58:59]
	s_mov_b32 m0, s1
	v_cvt_pk_f16_f32 v7, v6, v7
	global_load_lds_dwordx4 v[198:199], off
	v_cvt_pk_f16_f32 v6, v4, v5
	ds_write_b64 v100, v[6:7] offset:36864
	s_add_u32 s70, s22, 0x20f00
	s_addc_u32 s71, s90, 0
	s_setprio 1
	s_waitcnt lgkmcnt(1)
	v_mfma_f32_16x16x32_f16 v[68:71], v[226:229], v[202:205], v[68:71]
	v_mfma_f32_16x16x32_f16 v[64:67], v[226:229], v[206:209], v[64:67]
	v_mfma_f32_16x16x32_f16 v[84:87], v[226:229], v[210:213], v[84:87]
	v_mfma_f32_16x16x32_f16 v[120:123], v[226:229], v[214:217], v[120:123]
	v_mfma_f32_16x16x32_f16 v[124:127], v[238:241], v[202:205], v[124:127]
	v_mfma_f32_16x16x32_f16 v[134:137], v[238:241], v[214:217], v[134:137]
	v_mfma_f32_16x16x32_f16 v[138:141], v[238:241], v[206:209], v[138:141]
	v_mfma_f32_16x16x32_f16 v[142:145], v[238:241], v[210:213], v[142:145]
	s_setprio 0
	ds_read_b128 v[226:229], v129 offset:8192
	ds_read_b128 v[238:241], v129 offset:10240
	v_readfirstlane_b32 s70, v97
	v_lshl_add_u64 v[198:199], v[92:93], 0, s[60:61]
	s_mov_b32 m0, s70
	v_cvt_pk_f16_f32 v15, v14, v15
	global_load_lds_dwordx4 v[198:199], off
	v_cvt_pk_f16_f32 v14, v12, v13
	ds_write_b64 v100, v[14:15] offset:40960
	s_add_u32 s72, s22, 0x40f00
	s_addc_u32 s73, s90, 0
	s_add_u32 s100, s22, 0xf00
	s_addc_u32 s101, s90, 0
	global_load_dwordx4 v[0:3], v201, s[100:101] nt
	s_setprio 1
	s_waitcnt lgkmcnt(1)
	v_mfma_f32_16x16x32_f16 v[72:75], v[226:229], v[202:205], v[72:75]
	v_mfma_f32_16x16x32_f16 v[88:91], v[226:229], v[206:209], v[88:91]
	v_mfma_f32_16x16x32_f16 v[146:149], v[226:229], v[214:217], v[146:149]
	v_mfma_f32_16x16x32_f16 v[170:173], v[226:229], v[210:213], v[170:173]
	v_mfma_f32_16x16x32_f16 v[150:153], v[238:241], v[202:205], v[150:153]
	v_mfma_f32_16x16x32_f16 v[162:165], v[238:241], v[206:209], v[162:165]
	v_mfma_f32_16x16x32_f16 v[174:177], v[238:241], v[210:213], v[174:177]
	v_mfma_f32_16x16x32_f16 v[154:157], v[238:241], v[214:217], v[154:157]
	s_setprio 0
	ds_read_b128 v[226:229], v129 offset:12288
	ds_read_b128 v[238:241], v129 offset:14336
	v_readfirstlane_b32 s71, v98
	v_lshl_add_u64 v[92:93], v[92:93], 0, s[62:63]
	s_mov_b32 m0, s71
	v_cvt_pk_f16_f32 v19, v18, v19
	global_load_lds_dwordx4 v[92:93], off
	v_cvt_pk_f16_f32 v18, v16, v17
	ds_write_b64 v100, v[18:19] offset:45056
	s_add_u32 s72, s22, 0x60f00
	s_addc_u32 s73, s90, 0
	s_add_u32 s100, s22, 0x20f00
	s_addc_u32 s101, s90, 0
	global_load_dwordx4 v[4:7], v201, s[100:101] nt
	s_setprio 1
	s_waitcnt lgkmcnt(1)
	v_mfma_f32_16x16x32_f16 v[76:79], v[226:229], v[202:205], v[76:79]
	v_mfma_f32_16x16x32_f16 v[234:237], v[226:229], v[206:209], v[234:237]
	v_mfma_f32_16x16x32_f16 v[158:161], v[226:229], v[210:213], v[158:161]
	v_mfma_f32_16x16x32_f16 v[166:169], v[226:229], v[214:217], v[166:169]
	v_mfma_f32_16x16x32_f16 v[178:181], v[238:241], v[202:205], v[178:181]
	v_mfma_f32_16x16x32_f16 v[182:185], v[238:241], v[206:209], v[182:185]
	v_mfma_f32_16x16x32_f16 v[190:193], v[238:241], v[210:213], v[190:193]
	v_mfma_f32_16x16x32_f16 v[186:189], v[238:241], v[214:217], v[186:189]
	s_setprio 0
	ds_read_b128 v[202:205], v128
	ds_read_b128 v[206:209], v128 offset:2048
	ds_read_b128 v[210:213], v128 offset:4096
	ds_read_b128 v[214:217], v128 offset:6144
	ds_read_b128 v[226:229], v130
	ds_read_b128 v[238:241], v130 offset:2048
	v_cvt_pk_f16_f32 v23, v22, v23
	v_cvt_pk_f16_f32 v22, v20, v21
	ds_write_b64 v100, v[22:23] offset:49152
	s_add_u32 s72, s22, 0x80f00
	s_addc_u32 s73, s90, 0
	s_add_u32 s100, s22, 0x40f00
	s_addc_u32 s101, s90, 0
	global_load_dwordx4 v[12:15], v201, s[100:101] nt
	s_setprio 1
	s_waitcnt lgkmcnt(1)
	v_mfma_f32_16x16x32_f16 v[80:83], v[226:229], v[202:205], v[80:83]
	v_mfma_f32_16x16x32_f16 v[104:107], v[226:229], v[210:213], v[104:107]
	v_mfma_f32_16x16x32_f16 v[108:111], v[238:241], v[202:205], v[108:111]
	v_mfma_f32_16x16x32_f16 v[112:115], v[238:241], v[206:209], v[112:115]
	v_mfma_f32_16x16x32_f16 v[116:119], v[238:241], v[210:213], v[116:119]
	v_mfma_f32_16x16x32_f16 v[230:233], v[226:229], v[206:209], v[230:233]
	v_mfma_f32_16x16x32_f16 v[218:221], v[226:229], v[214:217], v[218:221]
	v_mfma_f32_16x16x32_f16 v[222:225], v[238:241], v[214:217], v[222:225]
	s_setprio 0
	ds_read_b128 v[226:229], v130 offset:4096
	ds_read_b128 v[238:241], v130 offset:6144
	v_cvt_pk_f16_f32 v27, v26, v27
	v_cvt_pk_f16_f32 v26, v24, v25
	ds_write_b64 v100, v[26:27] offset:53248
	s_add_u32 s72, s22, 0xa0f00
	s_addc_u32 s73, s90, 0
	s_add_u32 s100, s22, 0x60f00
	s_addc_u32 s101, s90, 0
	global_load_dwordx4 v[16:19], v201, s[100:101] nt
	s_setprio 1
	s_waitcnt lgkmcnt(1)
	v_mfma_f32_16x16x32_f16 v[68:71], v[226:229], v[202:205], v[68:71]
	v_mfma_f32_16x16x32_f16 v[64:67], v[226:229], v[206:209], v[64:67]
	v_mfma_f32_16x16x32_f16 v[84:87], v[226:229], v[210:213], v[84:87]
	v_mfma_f32_16x16x32_f16 v[120:123], v[226:229], v[214:217], v[120:123]
	v_mfma_f32_16x16x32_f16 v[124:127], v[238:241], v[202:205], v[124:127]
	v_mfma_f32_16x16x32_f16 v[134:137], v[238:241], v[214:217], v[134:137]
	v_mfma_f32_16x16x32_f16 v[138:141], v[238:241], v[206:209], v[138:141]
	v_mfma_f32_16x16x32_f16 v[142:145], v[238:241], v[210:213], v[142:145]
	s_setprio 0
	ds_read_b128 v[226:229], v130 offset:8192
	ds_read_b128 v[238:241], v130 offset:10240
	v_cvt_pk_f16_f32 v31, v30, v31
	v_cvt_pk_f16_f32 v30, v28, v29
	ds_write_b64 v100, v[30:31] offset:57344
	s_add_u32 s72, s22, 0xc0f00
	s_addc_u32 s73, s90, 0
	s_add_u32 s100, s22, 0x80f00
	s_addc_u32 s101, s90, 0
	global_load_dwordx4 v[20:23], v201, s[100:101] nt
	s_add_u32 s100, s22, 0xa0f00
	s_addc_u32 s101, s90, 0
	global_load_dwordx4 v[24:27], v201, s[100:101] nt
	s_setprio 1
	s_waitcnt lgkmcnt(1)
	v_mfma_f32_16x16x32_f16 v[72:75], v[226:229], v[202:205], v[72:75]
	v_mfma_f32_16x16x32_f16 v[88:91], v[226:229], v[206:209], v[88:91]
	v_mfma_f32_16x16x32_f16 v[146:149], v[226:229], v[214:217], v[146:149]
	v_mfma_f32_16x16x32_f16 v[170:173], v[226:229], v[210:213], v[170:173]
	v_mfma_f32_16x16x32_f16 v[150:153], v[238:241], v[202:205], v[150:153]
	v_mfma_f32_16x16x32_f16 v[162:165], v[238:241], v[206:209], v[162:165]
	v_mfma_f32_16x16x32_f16 v[174:177], v[238:241], v[210:213], v[174:177]
	v_mfma_f32_16x16x32_f16 v[154:157], v[238:241], v[214:217], v[154:157]
	s_setprio 0
	ds_read_b128 v[226:229], v130 offset:12288
	ds_read_b128 v[238:241], v130 offset:14336
	v_cvt_pk_f16_f32 v35, v34, v35
	v_cvt_pk_f16_f32 v34, v32, v33
	ds_write_b64 v100, v[34:35] offset:61440
	s_add_u32 s72, s22, 0xe0f00
	s_addc_u32 s73, s90, 0
	s_add_u32 s100, s22, 0xc0f00
	s_addc_u32 s101, s90, 0
	global_load_dwordx4 v[28:31], v201, s[100:101] nt
	s_add_u32 s100, s22, 0xe0f00
	s_addc_u32 s101, s90, 0
	global_load_dwordx4 v[32:35], v201, s[100:101] nt
	s_setprio 1
	s_waitcnt lgkmcnt(1)
	v_mfma_f32_16x16x32_f16 v[76:79], v[226:229], v[202:205], v[76:79]
	v_mfma_f32_16x16x32_f16 v[234:237], v[226:229], v[206:209], v[234:237]
	v_mfma_f32_16x16x32_f16 v[158:161], v[226:229], v[210:213], v[158:161]
	v_mfma_f32_16x16x32_f16 v[166:169], v[226:229], v[214:217], v[166:169]
	v_mfma_f32_16x16x32_f16 v[178:181], v[238:241], v[202:205], v[178:181]
	v_mfma_f32_16x16x32_f16 v[182:185], v[238:241], v[206:209], v[182:185]
	v_mfma_f32_16x16x32_f16 v[190:193], v[238:241], v[210:213], v[190:193]
	v_mfma_f32_16x16x32_f16 v[186:189], v[238:241], v[214:217], v[186:189]
	s_setprio 0
	s_waitcnt vmcnt(7)
	s_waitcnt lgkmcnt(0)
	s_barrier
	ds_read_b128 v[202:205], v131 offset:32768
	ds_read_b128 v[206:209], v131 offset:34816
	ds_read_b128 v[210:213], v131 offset:36864
	ds_read_b128 v[214:217], v131 offset:38912
	ds_read_b128 v[226:229], v129 offset:32768
	ds_read_b128 v[238:241], v129 offset:34816
	v_lshl_add_u64 v[198:199], s[54:55], 0, v[196:197]
	v_readfirstlane_b32 s64, v94
	s_mov_b32 m0, s64
	v_cvt_pk_f16_f32 v11, v10, v11
	global_load_lds_dwordx4 v[198:199], off
	v_cvt_pk_f16_f32 v10, v8, v9
	ds_write_b64 v100, v[10:11]
	s_setprio 1
	s_waitcnt lgkmcnt(1)
	v_mfma_f32_16x16x32_f16 v[8:11], v[226:229], v[202:205], v[80:83]
	v_mfma_f32_16x16x32_f16 v[80:83], v[226:229], v[206:209], v[230:233]
	v_mfma_f32_16x16x32_f16 v[92:95], v[226:229], v[210:213], v[104:107]
	v_mfma_f32_16x16x32_f16 v[104:107], v[226:229], v[214:217], v[218:221]
	v_mfma_f32_16x16x32_f16 v[108:111], v[238:241], v[202:205], v[108:111]
	v_mfma_f32_16x16x32_f16 v[112:115], v[238:241], v[206:209], v[112:115]
	v_mfma_f32_16x16x32_f16 v[116:119], v[238:241], v[210:213], v[116:119]
	v_mfma_f32_16x16x32_f16 v[218:221], v[238:241], v[214:217], v[222:225]
	s_setprio 0
	s_nop 1
	ds_read_b128 v[222:225], v129 offset:36864
	ds_read_b128 v[226:229], v129 offset:38912
	v_readfirstlane_b32 s64, v99
	v_lshl_add_u64 v[96:97], v[198:199], 0, s[58:59]
	s_mov_b32 m0, s64
	v_cvt_pk_f16_f32 v43, v42, v43
	global_load_lds_dwordx4 v[96:97], off
	v_cvt_pk_f16_f32 v42, v40, v41
	ds_write_b64 v100, v[42:43] offset:4096
	s_setprio 1
	s_waitcnt lgkmcnt(1)
	v_mfma_f32_16x16x32_f16 v[40:43], v[222:225], v[202:205], v[68:71]
	v_mfma_f32_16x16x32_f16 v[64:67], v[222:225], v[206:209], v[64:67]
	v_mfma_f32_16x16x32_f16 v[68:71], v[222:225], v[210:213], v[84:87]
	v_mfma_f32_16x16x32_f16 v[84:87], v[222:225], v[214:217], v[120:123]
	v_mfma_f32_16x16x32_f16 v[96:99], v[226:229], v[202:205], v[124:127]
	v_mfma_f32_16x16x32_f16 v[120:123], v[226:229], v[206:209], v[138:141]
	v_mfma_f32_16x16x32_f16 v[124:127], v[226:229], v[210:213], v[142:145]
	v_mfma_f32_16x16x32_f16 v[134:137], v[226:229], v[214:217], v[134:137]
	s_setprio 0
	ds_read_b128 v[138:141], v129 offset:40960
	ds_read_b128 v[142:145], v129 offset:43008
	v_readfirstlane_b32 s64, v101
	v_lshl_add_u64 v[222:223], v[198:199], 0, s[60:61]
	s_mov_b32 m0, s64
	v_cvt_pk_f16_f32 v47, v46, v47
	global_load_lds_dwordx4 v[222:223], off
	v_cvt_pk_f16_f32 v46, v44, v45
	ds_write_b64 v100, v[46:47] offset:8192
	s_setprio 1
	s_waitcnt lgkmcnt(1)
	v_mfma_f32_16x16x32_f16 v[44:47], v[138:141], v[202:205], v[72:75]
	v_mfma_f32_16x16x32_f16 v[72:75], v[138:141], v[206:209], v[88:91]
	v_mfma_f32_16x16x32_f16 v[88:91], v[138:141], v[210:213], v[170:173]
	v_mfma_f32_16x16x32_f16 v[138:141], v[138:141], v[214:217], v[146:149]
	v_mfma_f32_16x16x32_f16 v[146:149], v[142:145], v[202:205], v[150:153]
	v_mfma_f32_16x16x32_f16 v[150:153], v[142:145], v[206:209], v[162:165]
	v_mfma_f32_16x16x32_f16 v[162:165], v[142:145], v[210:213], v[174:177]
	v_mfma_f32_16x16x32_f16 v[142:145], v[142:145], v[214:217], v[154:157]
	s_setprio 0
	s_nop 1
	ds_read_b128 v[154:157], v129 offset:45056
	ds_read_b128 v[170:173], v129 offset:47104
	v_readfirstlane_b32 s64, v102
	v_lshl_add_u64 v[174:175], v[198:199], 0, s[62:63]
	s_mov_b32 m0, s64
	v_cvt_pk_f16_f32 v51, v50, v51
	global_load_lds_dwordx4 v[174:175], off
	v_cvt_pk_f16_f32 v50, v48, v49
	ds_write_b64 v100, v[50:51] offset:12288
	s_setprio 1
	s_waitcnt lgkmcnt(1)
	v_mfma_f32_16x16x32_f16 v[48:51], v[154:157], v[202:205], v[76:79]
	v_mfma_f32_16x16x32_f16 v[76:79], v[154:157], v[206:209], v[234:237]
	v_mfma_f32_16x16x32_f16 v[158:161], v[154:157], v[210:213], v[158:161]
	v_mfma_f32_16x16x32_f16 v[154:157], v[154:157], v[214:217], v[166:169]
	v_mfma_f32_16x16x32_f16 v[166:169], v[170:173], v[202:205], v[178:181]
	v_mfma_f32_16x16x32_f16 v[174:177], v[170:173], v[206:209], v[182:185]
	v_mfma_f32_16x16x32_f16 v[178:181], v[170:173], v[210:213], v[190:193]
	v_mfma_f32_16x16x32_f16 v[170:173], v[170:173], v[214:217], v[186:189]
	s_setprio 0
	ds_read_b128 v[182:185], v128 offset:32768
	s_nop 0
	ds_read_b128 v[186:189], v128 offset:34816
	ds_read_b128 v[190:193], v128 offset:36864
	ds_read_b128 v[202:205], v128 offset:38912
	ds_read_b128 v[206:209], v130 offset:32768
	ds_read_b128 v[210:213], v130 offset:34816
	v_cvt_pk_f16_f32 v55, v54, v55
	v_cvt_pk_f16_f32 v54, v52, v53
	ds_write_b64 v100, v[54:55] offset:16384
	s_setprio 1
	s_waitcnt lgkmcnt(1)
	v_mfma_f32_16x16x32_f16 v[8:11], v[206:209], v[182:185], v[8:11]
	v_mfma_f32_16x16x32_f16 v[52:55], v[206:209], v[186:189], v[80:83]
	v_mfma_f32_16x16x32_f16 v[80:83], v[206:209], v[190:193], v[92:95]
	v_mfma_f32_16x16x32_f16 v[92:95], v[206:209], v[202:205], v[104:107]
	v_mfma_f32_16x16x32_f16 v[102:105], v[210:213], v[182:185], v[108:111]
	v_mfma_f32_16x16x32_f16 v[106:109], v[210:213], v[186:189], v[112:115]
	v_mfma_f32_16x16x32_f16 v[110:113], v[210:213], v[190:193], v[116:119]
	v_mfma_f32_16x16x32_f16 v[114:117], v[210:213], v[202:205], v[218:221]
	s_setprio 0
	ds_read_b128 v[206:209], v130 offset:36864
	ds_read_b128 v[210:213], v130 offset:38912
	v_cvt_pk_f16_f32 v59, v58, v59
	v_cvt_pk_f16_f32 v58, v56, v57
	ds_write_b64 v100, v[58:59] offset:20480
	s_setprio 1
	s_waitcnt lgkmcnt(1)
	v_mfma_f32_16x16x32_f16 v[40:43], v[206:209], v[182:185], v[40:43]
	v_mfma_f32_16x16x32_f16 v[56:59], v[206:209], v[186:189], v[64:67]
	v_mfma_f32_16x16x32_f16 v[64:67], v[206:209], v[190:193], v[68:71]
	v_mfma_f32_16x16x32_f16 v[68:71], v[206:209], v[202:205], v[84:87]
	v_mfma_f32_16x16x32_f16 v[84:87], v[210:213], v[182:185], v[96:99]
	v_mfma_f32_16x16x32_f16 v[96:99], v[210:213], v[186:189], v[120:123]
	v_mfma_f32_16x16x32_f16 v[118:121], v[210:213], v[190:193], v[124:127]
	v_mfma_f32_16x16x32_f16 v[122:125], v[210:213], v[202:205], v[134:137]
	s_setprio 0
	s_nop 1
	ds_read_b128 v[134:137], v130 offset:40960
	ds_read_b128 v[206:209], v130 offset:43008
	v_cvt_pk_f16_f32 v63, v62, v63
	v_cvt_pk_f16_f32 v62, v60, v61
	ds_write_b64 v100, v[62:63] offset:24576
	s_setprio 1
	s_waitcnt lgkmcnt(1)
	v_mfma_f32_16x16x32_f16 v[44:47], v[134:137], v[182:185], v[44:47]
	v_mfma_f32_16x16x32_f16 v[60:63], v[134:137], v[186:189], v[72:75]
	v_mfma_f32_16x16x32_f16 v[72:75], v[134:137], v[190:193], v[88:91]
	v_mfma_f32_16x16x32_f16 v[88:91], v[134:137], v[202:205], v[138:141]
	v_mfma_f32_16x16x32_f16 v[134:137], v[206:209], v[182:185], v[146:149]
	v_mfma_f32_16x16x32_f16 v[146:149], v[206:209], v[190:193], v[162:165]
	v_mfma_f32_16x16x32_f16 v[138:141], v[206:209], v[186:189], v[150:153]
	v_mfma_f32_16x16x32_f16 v[142:145], v[206:209], v[202:205], v[142:145]
	s_setprio 0
	s_nop 0
	ds_read_b128 v[150:153], v130 offset:45056
	ds_read_b128 v[162:165], v130 offset:47104
	v_cvt_pk_f16_f32 v39, v38, v39
	v_cvt_pk_f16_f32 v38, v36, v37
	ds_write_b64 v100, v[38:39] offset:28672
	s_setprio 1
	s_waitcnt lgkmcnt(1)
	v_mfma_f32_16x16x32_f16 v[36:39], v[150:153], v[182:185], v[48:51]
	v_mfma_f32_16x16x32_f16 v[48:51], v[150:153], v[186:189], v[76:79]
	v_mfma_f32_16x16x32_f16 v[76:79], v[150:153], v[190:193], v[158:161]
	v_mfma_f32_16x16x32_f16 v[150:153], v[150:153], v[202:205], v[154:157]
	v_mfma_f32_16x16x32_f16 v[154:157], v[162:165], v[182:185], v[166:169]
	v_mfma_f32_16x16x32_f16 v[158:161], v[162:165], v[186:189], v[174:177]
	v_mfma_f32_16x16x32_f16 v[166:169], v[162:165], v[190:193], v[178:181]
	v_mfma_f32_16x16x32_f16 v[162:165], v[162:165], v[202:205], v[170:173]
	s_setprio 0
	s_waitcnt vmcnt(0)
	s_waitcnt lgkmcnt(0)
	s_barrier
	s_nop 0
	ds_read_b128 v[170:173], v131
	ds_read_b128 v[174:177], v131 offset:2048
	ds_read_b128 v[178:181], v131 offset:4096
	ds_read_b128 v[182:185], v131 offset:6144
	ds_read_b128 v[186:189], v129
	ds_read_b128 v[190:193], v129 offset:2048
	v_lshl_add_u64 v[126:127], s[56:57], 0, v[196:197]
	s_mov_b32 m0, s0
	v_cvt_pk_f16_f32 v3, v2, v3
	global_load_lds_dwordx4 v[126:127], off
	v_cvt_pk_f16_f32 v2, v0, v1
	ds_write_b64 v100, v[2:3] offset:32768
	s_setprio 1
	s_waitcnt lgkmcnt(1)
	v_mfma_f32_16x16x32_f16 v[0:3], v[186:189], v[170:173], v[8:11]
	v_mfma_f32_16x16x32_f16 v[8:11], v[186:189], v[174:177], v[52:55]
	v_mfma_f32_16x16x32_f16 v[52:55], v[186:189], v[178:181], v[80:83]
	v_mfma_f32_16x16x32_f16 v[80:83], v[186:189], v[182:185], v[92:95]
	v_mfma_f32_16x16x32_f16 v[92:95], v[190:193], v[170:173], v[102:105]
	v_mfma_f32_16x16x32_f16 v[102:105], v[190:193], v[174:177], v[106:109]
	v_mfma_f32_16x16x32_f16 v[106:109], v[190:193], v[178:181], v[110:113]
	v_mfma_f32_16x16x32_f16 v[110:113], v[190:193], v[182:185], v[114:117]
	s_setprio 0
	s_nop 1
	ds_read_b128 v[114:117], v129 offset:4096
	ds_read_b128 v[186:189], v129 offset:6144
	s_mov_b32 m0, s1
	v_lshl_add_u64 v[190:191], v[126:127], 0, s[58:59]
	global_load_lds_dwordx4 v[190:191], off
	v_cvt_pk_f16_f32 v7, v6, v7
	v_cvt_pk_f16_f32 v6, v4, v5
	ds_write_b64 v100, v[6:7] offset:36864
	s_setprio 1
	s_waitcnt lgkmcnt(1)
	v_mfma_f32_16x16x32_f16 v[190:193], v[114:117], v[170:173], v[40:43]
	v_mfma_f32_16x16x32_f16 v[56:59], v[114:117], v[174:177], v[56:59]
	v_mfma_f32_16x16x32_f16 v[64:67], v[114:117], v[178:181], v[64:67]
	v_mfma_f32_16x16x32_f16 v[68:71], v[114:117], v[182:185], v[68:71]
	v_mfma_f32_16x16x32_f16 v[84:87], v[186:189], v[170:173], v[84:87]
	v_mfma_f32_16x16x32_f16 v[96:99], v[186:189], v[174:177], v[96:99]
	v_mfma_f32_16x16x32_f16 v[114:117], v[186:189], v[178:181], v[118:121]
	v_mfma_f32_16x16x32_f16 v[118:121], v[186:189], v[182:185], v[122:125]
	s_setprio 0
	ds_read_b128 v[4:7], v129 offset:8192
	ds_read_b128 v[40:43], v129 offset:10240
	s_mov_b32 m0, s70
	v_lshl_add_u64 v[122:123], v[126:127], 0, s[60:61]
	global_load_lds_dwordx4 v[122:123], off
	v_cvt_pk_f16_f32 v15, v14, v15
	v_cvt_pk_f16_f32 v14, v12, v13
	ds_write_b64 v100, v[14:15] offset:40960
	s_setprio 1
	s_waitcnt lgkmcnt(1)
	v_mfma_f32_16x16x32_f16 v[122:125], v[4:7], v[170:173], v[44:47]
	v_mfma_f32_16x16x32_f16 v[88:91], v[4:7], v[182:185], v[88:91]
	v_mfma_f32_16x16x32_f16 v[134:137], v[40:43], v[170:173], v[134:137]
	v_mfma_f32_16x16x32_f16 v[146:149], v[40:43], v[178:181], v[146:149]
	v_mfma_f32_16x16x32_f16 v[186:189], v[4:7], v[174:177], v[60:63]
	v_mfma_f32_16x16x32_f16 v[202:205], v[4:7], v[178:181], v[72:75]
	v_mfma_f32_16x16x32_f16 v[138:141], v[40:43], v[174:177], v[138:141]
	v_mfma_f32_16x16x32_f16 v[142:145], v[40:43], v[182:185], v[142:145]
	s_setprio 0
	ds_read_b128 v[4:7], v129 offset:12288
	ds_read_b128 v[12:15], v129 offset:14336
	s_mov_b32 m0, s71
	v_lshl_add_u64 v[40:41], v[126:127], 0, s[62:63]
	global_load_lds_dwordx4 v[40:41], off
	v_cvt_pk_f16_f32 v19, v18, v19
	v_cvt_pk_f16_f32 v18, v16, v17
	ds_write_b64 v100, v[18:19] offset:45056
	s_setprio 1
	s_waitcnt lgkmcnt(1)
	v_mfma_f32_16x16x32_f16 v[206:209], v[4:7], v[170:173], v[36:39]
	v_mfma_f32_16x16x32_f16 v[210:213], v[4:7], v[174:177], v[48:51]
	v_mfma_f32_16x16x32_f16 v[214:217], v[4:7], v[178:181], v[76:79]
	v_mfma_f32_16x16x32_f16 v[150:153], v[4:7], v[182:185], v[150:153]
	v_mfma_f32_16x16x32_f16 v[154:157], v[12:15], v[170:173], v[154:157]
	v_mfma_f32_16x16x32_f16 v[158:161], v[12:15], v[174:177], v[158:161]
	v_mfma_f32_16x16x32_f16 v[166:169], v[12:15], v[178:181], v[166:169]
	v_mfma_f32_16x16x32_f16 v[162:165], v[12:15], v[182:185], v[162:165]
	s_setprio 0
	ds_read_b128 v[170:173], v128
	ds_read_b128 v[174:177], v128 offset:2048
	ds_read_b128 v[178:181], v128 offset:4096
	ds_read_b128 v[182:185], v128 offset:6144
	ds_read_b128 v[12:15], v130
	ds_read_b128 v[40:43], v130 offset:2048
	v_cvt_pk_f16_f32 v5, v22, v23
	v_cvt_pk_f16_f32 v4, v20, v21
	ds_write_b64 v100, v[4:5] offset:49152
	s_setprio 1
	s_waitcnt lgkmcnt(1)
	v_mfma_f32_16x16x32_f16 v[0:3], v[12:15], v[170:173], v[0:3]
	v_mfma_f32_16x16x32_f16 v[4:7], v[12:15], v[174:177], v[8:11]
	v_mfma_f32_16x16x32_f16 v[8:11], v[12:15], v[178:181], v[52:55]
	v_mfma_f32_16x16x32_f16 v[12:15], v[12:15], v[182:185], v[80:83]
	v_mfma_f32_16x16x32_f16 v[16:19], v[40:43], v[170:173], v[92:95]
	v_mfma_f32_16x16x32_f16 v[20:23], v[40:43], v[174:177], v[102:105]
	v_mfma_f32_16x16x32_f16 v[36:39], v[40:43], v[178:181], v[106:109]
	v_mfma_f32_16x16x32_f16 v[40:43], v[40:43], v[182:185], v[110:113]
	s_setprio 0
	ds_read_b128 v[52:55], v130 offset:4096
	ds_read_b128 v[72:75], v130 offset:6144
	v_cvt_pk_f16_f32 v27, v26, v27
	v_cvt_pk_f16_f32 v26, v24, v25
	ds_write_b64 v100, v[26:27] offset:53248
	s_setprio 1
	s_waitcnt lgkmcnt(1)
	v_mfma_f32_16x16x32_f16 v[24:27], v[52:55], v[170:173], v[190:193]
	v_mfma_f32_16x16x32_f16 v[44:47], v[52:55], v[174:177], v[56:59]
	v_mfma_f32_16x16x32_f16 v[48:51], v[52:55], v[178:181], v[64:67]
	v_mfma_f32_16x16x32_f16 v[52:55], v[52:55], v[182:185], v[68:71]
	v_mfma_f32_16x16x32_f16 v[56:59], v[72:75], v[170:173], v[84:87]
	v_mfma_f32_16x16x32_f16 v[60:63], v[72:75], v[174:177], v[96:99]
	v_mfma_f32_16x16x32_f16 v[64:67], v[72:75], v[178:181], v[114:117]
	v_mfma_f32_16x16x32_f16 v[68:71], v[72:75], v[182:185], v[118:121]
	s_setprio 0
	ds_read_b128 v[80:83], v130 offset:8192
	ds_read_b128 v[96:99], v130 offset:10240
	v_cvt_pk_f16_f32 v31, v30, v31
	v_cvt_pk_f16_f32 v30, v28, v29
	ds_write_b64 v100, v[30:31] offset:57344
	s_setprio 1
	s_waitcnt lgkmcnt(1)
	v_mfma_f32_16x16x32_f16 v[28:31], v[80:83], v[170:173], v[122:125]
	v_mfma_f32_16x16x32_f16 v[72:75], v[80:83], v[174:177], v[186:189]
	v_mfma_f32_16x16x32_f16 v[76:79], v[80:83], v[178:181], v[202:205]
	v_mfma_f32_16x16x32_f16 v[80:83], v[80:83], v[182:185], v[88:91]
	v_mfma_f32_16x16x32_f16 v[84:87], v[96:99], v[170:173], v[134:137]
	v_mfma_f32_16x16x32_f16 v[88:91], v[96:99], v[174:177], v[138:141]
	v_mfma_f32_16x16x32_f16 v[92:95], v[96:99], v[178:181], v[146:149]
	v_mfma_f32_16x16x32_f16 v[96:99], v[96:99], v[182:185], v[142:145]
	s_setprio 0
	ds_read_b128 v[108:111], v130 offset:12288
	ds_read_b128 v[124:127], v130 offset:14336
	v_cvt_pk_f16_f32 v35, v34, v35
	v_cvt_pk_f16_f32 v34, v32, v33
	ds_write_b64 v100, v[34:35] offset:61440
	s_setprio 1
	s_waitcnt lgkmcnt(1)
	v_mfma_f32_16x16x32_f16 v[32:35], v[108:111], v[170:173], v[206:209]
	v_mfma_f32_16x16x32_f16 v[100:103], v[108:111], v[174:177], v[210:213]
	v_mfma_f32_16x16x32_f16 v[104:107], v[108:111], v[178:181], v[214:217]
	v_mfma_f32_16x16x32_f16 v[108:111], v[108:111], v[182:185], v[150:153]
	v_mfma_f32_16x16x32_f16 v[112:115], v[124:127], v[170:173], v[154:157]
	v_mfma_f32_16x16x32_f16 v[116:119], v[124:127], v[174:177], v[158:161]
	v_mfma_f32_16x16x32_f16 v[120:123], v[124:127], v[178:181], v[166:169]
	v_mfma_f32_16x16x32_f16 v[124:127], v[124:127], v[182:185], v[162:165]
	s_setprio 0
	s_waitcnt vmcnt(0)
	s_waitcnt lgkmcnt(0)
	s_barrier
	ds_read_b128 v[134:137], v131 offset:32768
	ds_read_b128 v[138:141], v131 offset:34816
	ds_read_b128 v[142:145], v131 offset:36864
	ds_read_b128 v[148:151], v131 offset:38912
	ds_read_b128 v[152:155], v129 offset:32768
	ds_read_b128 v[156:159], v129 offset:34816
	s_setprio 1
	s_waitcnt lgkmcnt(0)
	v_mfma_f32_16x16x32_f16 v[0:3], v[152:155], v[134:137], v[0:3]
	v_mfma_f32_16x16x32_f16 v[4:7], v[152:155], v[138:141], v[4:7]
	v_mfma_f32_16x16x32_f16 v[8:11], v[152:155], v[142:145], v[8:11]
	v_mfma_f32_16x16x32_f16 v[12:15], v[152:155], v[148:151], v[12:15]
	v_mfma_f32_16x16x32_f16 v[16:19], v[156:159], v[134:137], v[16:19]
	v_mfma_f32_16x16x32_f16 v[20:23], v[156:159], v[138:141], v[20:23]
	v_mfma_f32_16x16x32_f16 v[36:39], v[156:159], v[142:145], v[36:39]
	v_mfma_f32_16x16x32_f16 v[40:43], v[156:159], v[148:151], v[40:43]
	s_setprio 0
	ds_read_b128 v[152:155], v129 offset:36864
	ds_read_b128 v[156:159], v129 offset:38912
	v_and_b32_e32 v250, 0x7ffffc00, v194
	v_lshl_add_u64 v[252:253], s[10:11], 0, v[196:197]
	v_readfirstlane_b32 s32, v250
	s_nop 0
	s_mov_b32 m0, s32
	s_nop 0
	global_load_lds_dwordx4 v[252:253], off
	v_mov_b32_e32 v146, 0
	v_and_b32_e32 v251, 0xfffffff, v132
	v_cmp_gt_u32_e32 vcc, s82, v251
	v_mov_b32_e32 v132, 0
	v_mov_b32_e32 v133, 0
	s_and_saveexec_b64 s[0:1], vcc
	s_cbranch_execz .LBB1_7
	s_and_b32 s64, s78, 0x7ffffc00
	s_or_b32 s64, s64, s33
	v_or_b32_e32 v132, s64, v251
	v_mov_b32_e32 v133, v195
	v_lshl_add_u64 v[132:133], v[132:133], 2, s[12:13]
	global_load_dword v133, v[132:133], off
	v_or_b32_e32 v132, s33, v251
	v_lshlrev_b32_e32 v132, 2, v132
	global_load_dword v146, v132, s[16:17]
	s_nop 0
	global_load_dword v132, v132, s[14:15]
